# stacked version with every s_setprio of the GEMM loops deleted (timing-only change)
# baseline (speedup 1.0000x reference)
.Lwa_186p_0:
	s_waitcnt lgkmcnt(0)
	s_barrier
	s_waitcnt lgkmcnt(0)
	v_mfma_scale_f32_16x16x128_f8f6f4 v[158:161], v[26:33], v[196:203], 0, v194, v194 op_sel_hi:[0,0,0]
	v_mfma_scale_f32_16x16x128_f8f6f4 v[154:157], v[18:25], v[196:203], 0, v194, v194 op_sel_hi:[0,0,0]
	v_mfma_scale_f32_16x16x128_f8f6f4 v[142:145], v[26:33], v[204:211], 0, v194, v194 op_sel_hi:[0,0,0]
	v_mfma_scale_f32_16x16x128_f8f6f4 v[138:141], v[18:25], v[204:211], 0, v194, v194 op_sel_hi:[0,0,0]
	v_mfma_scale_f32_16x16x128_f8f6f4 v[126:129], v[26:33], v[212:219], 0, v194, v194 op_sel_hi:[0,0,0]
	v_mfma_scale_f32_16x16x128_f8f6f4 v[122:125], v[18:25], v[212:219], 0, v194, v194 op_sel_hi:[0,0,0]
	v_mfma_scale_f32_16x16x128_f8f6f4 v[110:113], v[26:33], v[220:227], 0, v194, v194 op_sel_hi:[0,0,0]
	v_mfma_scale_f32_16x16x128_f8f6f4 v[106:109], v[18:25], v[220:227], 0, v194, v194 op_sel_hi:[0,0,0]
	v_mfma_scale_f32_16x16x128_f8f6f4 v[150:153], v[10:17], v[196:203], 0, v194, v194 op_sel_hi:[0,0,0]
	v_mfma_scale_f32_16x16x128_f8f6f4 v[146:149], v[2:9], v[196:203], 0, v194, v194 op_sel_hi:[0,0,0]
	v_mfma_scale_f32_16x16x128_f8f6f4 v[134:137], v[10:17], v[204:211], 0, v194, v194 op_sel_hi:[0,0,0]
	v_mfma_scale_f32_16x16x128_f8f6f4 v[130:133], v[2:9], v[204:211], 0, v194, v194 op_sel_hi:[0,0,0]
	v_mfma_scale_f32_16x16x128_f8f6f4 v[118:121], v[10:17], v[212:219], 0, v194, v194 op_sel_hi:[0,0,0]
	v_mfma_scale_f32_16x16x128_f8f6f4 v[114:117], v[2:9], v[212:219], 0, v194, v194 op_sel_hi:[0,0,0]
	v_mfma_scale_f32_16x16x128_f8f6f4 v[102:105], v[10:17], v[220:227], 0, v194, v194 op_sel_hi:[0,0,0]
	v_mfma_scale_f32_16x16x128_f8f6f4 v[98:101], v[2:9], v[220:227], 0, v194, v194 op_sel_hi:[0,0,0]
	s_cbranch_vccz .Lwb_186p_0
	s_waitcnt vmcnt(8)
.Lwb_186p_0:
	s_barrier
	s_add_i32 s0, s49, s40
	v_lshl_add_u64 v[184:185], s[34:35], 0, v[164:165]
	s_mov_b32 m0, s0
	ds_read_b128 v[196:199], v193 offset:16384
	ds_read_b128 v[200:203], v193 offset:17408
	ds_read_b128 v[204:207], v193 offset:18432
	ds_read_b128 v[208:211], v193 offset:19456
	ds_read_b128 v[212:215], v193 offset:20480
	ds_read_b128 v[216:219], v193 offset:21504
	ds_read_b128 v[220:223], v193 offset:22528
	ds_read_b128 v[224:227], v193 offset:23552
	global_load_lds_dwordx4 v[184:185], off
	s_add_i32 m0, s0, 0x2000
	s_add_u32 s56, s34, 0x40000
	v_lshl_add_u64 v[184:185], s[34:35], 0, v[168:169]
	s_addc_u32 s57, s35, 0
	s_add_i32 s0, s50, s40
	global_load_lds_dwordx4 v[184:185], off
	v_lshl_add_u64 v[184:185], s[56:57], 0, v[164:165]
	s_mov_b32 m0, s0
	v_lshl_add_u64 v[186:187], s[36:37], 0, v[166:167]
	global_load_lds_dwordx4 v[184:185], off
	v_lshl_add_u64 v[184:185], s[56:57], 0, v[168:169]
	s_add_i32 m0, s0, 0x2000
	s_nop 0
	global_load_lds_dwordx4 v[184:185], off
	v_lshl_add_u64 v[184:185], s[36:37], 0, v[162:163]
	s_mov_b32 m0, s29
	s_nop 0
	global_load_lds_dwordx4 v[184:185], off
	s_mov_b32 m0, s41
	s_nop 0
	global_load_lds_dwordx4 v[186:187], off
	s_and_b64 vcc, exec, s[14:15]
	s_cbranch_vccnz .Lwa_186p_1
	s_waitcnt vmcnt(8)
.Lwa_186p_1:
	s_waitcnt lgkmcnt(0)
	s_barrier
	s_waitcnt lgkmcnt(0)
	v_mfma_scale_f32_16x16x128_f8f6f4 v[94:97], v[26:33], v[196:203], 0, v194, v194 op_sel_hi:[0,0,0]
	v_mfma_scale_f32_16x16x128_f8f6f4 v[90:93], v[18:25], v[196:203], 0, v194, v194 op_sel_hi:[0,0,0]
	v_mfma_scale_f32_16x16x128_f8f6f4 v[78:81], v[26:33], v[204:211], 0, v194, v194 op_sel_hi:[0,0,0]
	v_mfma_scale_f32_16x16x128_f8f6f4 v[74:77], v[18:25], v[204:211], 0, v194, v194 op_sel_hi:[0,0,0]
	v_mfma_scale_f32_16x16x128_f8f6f4 v[62:65], v[26:33], v[212:219], 0, v194, v194 op_sel_hi:[0,0,0]
	v_mfma_scale_f32_16x16x128_f8f6f4 v[58:61], v[18:25], v[212:219], 0, v194, v194 op_sel_hi:[0,0,0]
	v_mfma_scale_f32_16x16x128_f8f6f4 v[46:49], v[26:33], v[220:227], 0, v194, v194 op_sel_hi:[0,0,0]
	v_mfma_scale_f32_16x16x128_f8f6f4 v[42:45], v[18:25], v[220:227], 0, v194, v194 op_sel_hi:[0,0,0]
	v_mfma_scale_f32_16x16x128_f8f6f4 v[86:89], v[10:17], v[196:203], 0, v194, v194 op_sel_hi:[0,0,0]
	v_mfma_scale_f32_16x16x128_f8f6f4 v[82:85], v[2:9], v[196:203], 0, v194, v194 op_sel_hi:[0,0,0]
	v_mfma_scale_f32_16x16x128_f8f6f4 v[70:73], v[10:17], v[204:211], 0, v194, v194 op_sel_hi:[0,0,0]
	v_mfma_scale_f32_16x16x128_f8f6f4 v[66:69], v[2:9], v[204:211], 0, v194, v194 op_sel_hi:[0,0,0]
	v_mfma_scale_f32_16x16x128_f8f6f4 v[54:57], v[10:17], v[212:219], 0, v194, v194 op_sel_hi:[0,0,0]
	v_mfma_scale_f32_16x16x128_f8f6f4 v[50:53], v[2:9], v[212:219], 0, v194, v194 op_sel_hi:[0,0,0]
	v_mfma_scale_f32_16x16x128_f8f6f4 v[38:41], v[10:17], v[220:227], 0, v194, v194 op_sel_hi:[0,0,0]
	v_mfma_scale_f32_16x16x128_f8f6f4 v[34:37], v[2:9], v[220:227], 0, v194, v194 op_sel_hi:[0,0,0]
	s_cbranch_vccz .Lwb_186p_1
	s_waitcnt vmcnt(8)
.Lwb_186p_1:
	s_barrier
	s_branch .Lmid_186

.Lwa_186l_0:
	s_waitcnt lgkmcnt(0)
	s_barrier
	s_waitcnt lgkmcnt(0)
	v_mfma_scale_f32_16x16x128_f8f6f4 v[158:161], v[26:33], v[196:203], v[158:161], v194, v194 op_sel_hi:[0,0,0]
	v_mfma_scale_f32_16x16x128_f8f6f4 v[154:157], v[18:25], v[196:203], v[154:157], v194, v194 op_sel_hi:[0,0,0]
	v_mfma_scale_f32_16x16x128_f8f6f4 v[142:145], v[26:33], v[204:211], v[142:145], v194, v194 op_sel_hi:[0,0,0]
	v_mfma_scale_f32_16x16x128_f8f6f4 v[138:141], v[18:25], v[204:211], v[138:141], v194, v194 op_sel_hi:[0,0,0]
	v_mfma_scale_f32_16x16x128_f8f6f4 v[126:129], v[26:33], v[212:219], v[126:129], v194, v194 op_sel_hi:[0,0,0]
	v_mfma_scale_f32_16x16x128_f8f6f4 v[122:125], v[18:25], v[212:219], v[122:125], v194, v194 op_sel_hi:[0,0,0]
	v_mfma_scale_f32_16x16x128_f8f6f4 v[110:113], v[26:33], v[220:227], v[110:113], v194, v194 op_sel_hi:[0,0,0]
	v_mfma_scale_f32_16x16x128_f8f6f4 v[106:109], v[18:25], v[220:227], v[106:109], v194, v194 op_sel_hi:[0,0,0]
	v_mfma_scale_f32_16x16x128_f8f6f4 v[150:153], v[10:17], v[196:203], v[150:153], v194, v194 op_sel_hi:[0,0,0]
	v_mfma_scale_f32_16x16x128_f8f6f4 v[146:149], v[2:9], v[196:203], v[146:149], v194, v194 op_sel_hi:[0,0,0]
	v_mfma_scale_f32_16x16x128_f8f6f4 v[134:137], v[10:17], v[204:211], v[134:137], v194, v194 op_sel_hi:[0,0,0]
	v_mfma_scale_f32_16x16x128_f8f6f4 v[130:133], v[2:9], v[204:211], v[130:133], v194, v194 op_sel_hi:[0,0,0]
	v_mfma_scale_f32_16x16x128_f8f6f4 v[118:121], v[10:17], v[212:219], v[118:121], v194, v194 op_sel_hi:[0,0,0]
	v_mfma_scale_f32_16x16x128_f8f6f4 v[114:117], v[2:9], v[212:219], v[114:117], v194, v194 op_sel_hi:[0,0,0]
	v_mfma_scale_f32_16x16x128_f8f6f4 v[102:105], v[10:17], v[220:227], v[102:105], v194, v194 op_sel_hi:[0,0,0]
	v_mfma_scale_f32_16x16x128_f8f6f4 v[98:101], v[2:9], v[220:227], v[98:101], v194, v194 op_sel_hi:[0,0,0]
	s_cbranch_vccz .Lwb_186l_0
	s_waitcnt vmcnt(8)

.Lwa_186l_1:
	s_waitcnt lgkmcnt(0)
	s_barrier
	s_waitcnt lgkmcnt(0)
	v_mfma_scale_f32_16x16x128_f8f6f4 v[94:97], v[26:33], v[196:203], v[94:97], v194, v194 op_sel_hi:[0,0,0]
	v_mfma_scale_f32_16x16x128_f8f6f4 v[90:93], v[18:25], v[196:203], v[90:93], v194, v194 op_sel_hi:[0,0,0]
	v_mfma_scale_f32_16x16x128_f8f6f4 v[78:81], v[26:33], v[204:211], v[78:81], v194, v194 op_sel_hi:[0,0,0]
	v_mfma_scale_f32_16x16x128_f8f6f4 v[74:77], v[18:25], v[204:211], v[74:77], v194, v194 op_sel_hi:[0,0,0]
	v_mfma_scale_f32_16x16x128_f8f6f4 v[62:65], v[26:33], v[212:219], v[62:65], v194, v194 op_sel_hi:[0,0,0]
	v_mfma_scale_f32_16x16x128_f8f6f4 v[58:61], v[18:25], v[212:219], v[58:61], v194, v194 op_sel_hi:[0,0,0]
	v_mfma_scale_f32_16x16x128_f8f6f4 v[46:49], v[26:33], v[220:227], v[46:49], v194, v194 op_sel_hi:[0,0,0]
	v_mfma_scale_f32_16x16x128_f8f6f4 v[42:45], v[18:25], v[220:227], v[42:45], v194, v194 op_sel_hi:[0,0,0]
	v_mfma_scale_f32_16x16x128_f8f6f4 v[86:89], v[10:17], v[196:203], v[86:89], v194, v194 op_sel_hi:[0,0,0]
	v_mfma_scale_f32_16x16x128_f8f6f4 v[82:85], v[2:9], v[196:203], v[82:85], v194, v194 op_sel_hi:[0,0,0]
	v_mfma_scale_f32_16x16x128_f8f6f4 v[70:73], v[10:17], v[204:211], v[70:73], v194, v194 op_sel_hi:[0,0,0]
	v_mfma_scale_f32_16x16x128_f8f6f4 v[66:69], v[2:9], v[204:211], v[66:69], v194, v194 op_sel_hi:[0,0,0]
	v_mfma_scale_f32_16x16x128_f8f6f4 v[54:57], v[10:17], v[212:219], v[54:57], v194, v194 op_sel_hi:[0,0,0]
	v_mfma_scale_f32_16x16x128_f8f6f4 v[50:53], v[2:9], v[212:219], v[50:53], v194, v194 op_sel_hi:[0,0,0]
	v_mfma_scale_f32_16x16x128_f8f6f4 v[38:41], v[10:17], v[220:227], v[38:41], v194, v194 op_sel_hi:[0,0,0]
	v_mfma_scale_f32_16x16x128_f8f6f4 v[34:37], v[2:9], v[220:227], v[34:37], v194, v194 op_sel_hi:[0,0,0]
	s_cbranch_vccz .Lwb_186l_1
	s_waitcnt vmcnt(8)
.Lwb_186l_1:
	s_barrier

.Lwa_186l_2:
	s_waitcnt lgkmcnt(0)
	s_barrier
	s_waitcnt lgkmcnt(0)
	v_mfma_scale_f32_16x16x128_f8f6f4 v[158:161], v[2:9], v[196:203], v[158:161], v194, v194 op_sel_hi:[0,0,0]
	v_mfma_scale_f32_16x16x128_f8f6f4 v[154:157], v[10:17], v[196:203], v[154:157], v194, v194 op_sel_hi:[0,0,0]
	v_mfma_scale_f32_16x16x128_f8f6f4 v[142:145], v[2:9], v[204:211], v[142:145], v194, v194 op_sel_hi:[0,0,0]
	v_mfma_scale_f32_16x16x128_f8f6f4 v[138:141], v[10:17], v[204:211], v[138:141], v194, v194 op_sel_hi:[0,0,0]
	v_mfma_scale_f32_16x16x128_f8f6f4 v[126:129], v[2:9], v[212:219], v[126:129], v194, v194 op_sel_hi:[0,0,0]
	v_mfma_scale_f32_16x16x128_f8f6f4 v[122:125], v[10:17], v[212:219], v[122:125], v194, v194 op_sel_hi:[0,0,0]
	v_mfma_scale_f32_16x16x128_f8f6f4 v[110:113], v[2:9], v[220:227], v[110:113], v194, v194 op_sel_hi:[0,0,0]
	v_mfma_scale_f32_16x16x128_f8f6f4 v[106:109], v[10:17], v[220:227], v[106:109], v194, v194 op_sel_hi:[0,0,0]
	v_mfma_scale_f32_16x16x128_f8f6f4 v[150:153], v[18:25], v[196:203], v[150:153], v194, v194 op_sel_hi:[0,0,0]
	v_mfma_scale_f32_16x16x128_f8f6f4 v[146:149], v[26:33], v[196:203], v[146:149], v194, v194 op_sel_hi:[0,0,0]
	v_mfma_scale_f32_16x16x128_f8f6f4 v[134:137], v[18:25], v[204:211], v[134:137], v194, v194 op_sel_hi:[0,0,0]
	v_mfma_scale_f32_16x16x128_f8f6f4 v[130:133], v[26:33], v[204:211], v[130:133], v194, v194 op_sel_hi:[0,0,0]
	v_mfma_scale_f32_16x16x128_f8f6f4 v[118:121], v[18:25], v[212:219], v[118:121], v194, v194 op_sel_hi:[0,0,0]
	v_mfma_scale_f32_16x16x128_f8f6f4 v[114:117], v[26:33], v[212:219], v[114:117], v194, v194 op_sel_hi:[0,0,0]
	v_mfma_scale_f32_16x16x128_f8f6f4 v[102:105], v[18:25], v[220:227], v[102:105], v194, v194 op_sel_hi:[0,0,0]
	v_mfma_scale_f32_16x16x128_f8f6f4 v[98:101], v[26:33], v[220:227], v[98:101], v194, v194 op_sel_hi:[0,0,0]
	s_cbranch_vccz .Lwb_186l_2
	s_waitcnt vmcnt(8)
.Lwb_186l_2:
	s_barrier
	s_add_u32 s36, s34, 0x2000
	s_addc_u32 s37, s35, 0
	s_add_i32 s0, s0, s40
	v_lshl_add_u64 v[228:229], s[36:37], 0, v[164:165]
	s_mov_b32 m0, s0
	ds_read_b128 v[196:199], v193 offset:49152
	ds_read_b128 v[200:203], v193 offset:50176
	ds_read_b128 v[204:207], v193 offset:51200
	ds_read_b128 v[208:211], v193 offset:52224
	ds_read_b128 v[212:215], v193 offset:53248
	ds_read_b128 v[216:219], v193 offset:54272
	ds_read_b128 v[220:223], v193 offset:55296
	ds_read_b128 v[224:227], v193 offset:56320
	global_load_lds_dwordx4 v[228:229], off
	s_add_i32 m0, s0, 0x2000
	s_add_u32 s34, s34, 0x42000
	v_lshl_add_u64 v[228:229], s[36:37], 0, v[168:169]
	s_addc_u32 s35, s35, 0
	s_add_i32 s0, s1, s40
	global_load_lds_dwordx4 v[228:229], off
	v_lshl_add_u64 v[228:229], s[34:35], 0, v[164:165]
	s_mov_b32 m0, s0
	v_lshl_add_u64 v[184:185], v[184:185], 0, s[12:13]
	global_load_lds_dwordx4 v[228:229], off
	v_lshl_add_u64 v[228:229], s[34:35], 0, v[168:169]
	s_add_i32 m0, s0, 0x2000
	s_nop 0
	global_load_lds_dwordx4 v[228:229], off
	s_mov_b32 m0, s44
	s_nop 0
	global_load_lds_dwordx4 v[184:185], off
	v_lshl_add_u64 v[184:185], v[186:187], 0, s[12:13]
	s_mov_b32 m0, s45
	s_nop 0
	global_load_lds_dwordx4 v[184:185], off
	s_and_b64 vcc, exec, s[14:15]
	s_cbranch_vccnz .Lwa_186l_3
	s_waitcnt vmcnt(8)
.Lwa_186l_3:
	s_waitcnt lgkmcnt(0)
	s_barrier
	s_waitcnt lgkmcnt(0)
	v_mfma_scale_f32_16x16x128_f8f6f4 v[94:97], v[2:9], v[196:203], v[94:97], v194, v194 op_sel_hi:[0,0,0]
	v_mfma_scale_f32_16x16x128_f8f6f4 v[90:93], v[10:17], v[196:203], v[90:93], v194, v194 op_sel_hi:[0,0,0]
	v_mfma_scale_f32_16x16x128_f8f6f4 v[78:81], v[2:9], v[204:211], v[78:81], v194, v194 op_sel_hi:[0,0,0]
	v_mfma_scale_f32_16x16x128_f8f6f4 v[74:77], v[10:17], v[204:211], v[74:77], v194, v194 op_sel_hi:[0,0,0]
	v_mfma_scale_f32_16x16x128_f8f6f4 v[62:65], v[2:9], v[212:219], v[62:65], v194, v194 op_sel_hi:[0,0,0]
	v_mfma_scale_f32_16x16x128_f8f6f4 v[58:61], v[10:17], v[212:219], v[58:61], v194, v194 op_sel_hi:[0,0,0]
	v_mfma_scale_f32_16x16x128_f8f6f4 v[46:49], v[2:9], v[220:227], v[46:49], v194, v194 op_sel_hi:[0,0,0]
	v_mfma_scale_f32_16x16x128_f8f6f4 v[42:45], v[10:17], v[220:227], v[42:45], v194, v194 op_sel_hi:[0,0,0]
	v_mfma_scale_f32_16x16x128_f8f6f4 v[86:89], v[18:25], v[196:203], v[86:89], v194, v194 op_sel_hi:[0,0,0]
	v_mfma_scale_f32_16x16x128_f8f6f4 v[82:85], v[26:33], v[196:203], v[82:85], v194, v194 op_sel_hi:[0,0,0]
	v_mfma_scale_f32_16x16x128_f8f6f4 v[70:73], v[18:25], v[204:211], v[70:73], v194, v194 op_sel_hi:[0,0,0]
	v_mfma_scale_f32_16x16x128_f8f6f4 v[66:69], v[26:33], v[204:211], v[66:69], v194, v194 op_sel_hi:[0,0,0]
	v_mfma_scale_f32_16x16x128_f8f6f4 v[54:57], v[18:25], v[212:219], v[54:57], v194, v194 op_sel_hi:[0,0,0]
	v_mfma_scale_f32_16x16x128_f8f6f4 v[50:53], v[26:33], v[212:219], v[50:53], v194, v194 op_sel_hi:[0,0,0]
	v_mfma_scale_f32_16x16x128_f8f6f4 v[38:41], v[18:25], v[220:227], v[38:41], v194, v194 op_sel_hi:[0,0,0]
	v_mfma_scale_f32_16x16x128_f8f6f4 v[34:37], v[26:33], v[220:227], v[34:37], v194, v194 op_sel_hi:[0,0,0]
	s_cbranch_vccz .Lwb_186l_3
	s_waitcnt vmcnt(8)
.Lwb_186l_3:
	s_barrier
	s_add_i32 s55, s55, 2
	s_add_u32 s53, s53, 0x4000
	s_addc_u32 s54, s54, 0
	s_add_u32 s30, s30, 0x100
	s_addc_u32 s31, s31, 0
	s_cmp_gt_u32 s55, 13
	s_cbranch_scc0 .LBB0_186
	s_and_b64 vcc, exec, s[14:15]
	s_cbranch_vccz .LBB0_189
	s_barrier

.Lwa_1129p_0:
	s_waitcnt lgkmcnt(0)
	s_barrier
	s_waitcnt lgkmcnt(0)
	v_mfma_f32_16x16x32_bf16 v[126:129], v[146:149], v[192:195], 0
	v_mfma_f32_16x16x32_bf16 v[122:125], v[168:171], v[192:195], 0
	v_mfma_f32_16x16x32_bf16 v[110:113], v[146:149], v[200:203], 0
	v_mfma_f32_16x16x32_bf16 v[106:109], v[168:171], v[200:203], 0
	v_mfma_f32_16x16x32_bf16 v[94:97], v[146:149], v[208:211], 0
	v_mfma_f32_16x16x32_bf16 v[90:93], v[168:171], v[208:211], 0
	v_mfma_f32_16x16x32_bf16 v[78:81], v[146:149], v[216:219], 0
	v_mfma_f32_16x16x32_bf16 v[74:77], v[168:171], v[216:219], 0
	v_mfma_f32_16x16x32_bf16 v[126:129], v[150:153], v[196:199], v[126:129]
	v_mfma_f32_16x16x32_bf16 v[122:125], v[172:175], v[196:199], v[122:125]
	v_mfma_f32_16x16x32_bf16 v[110:113], v[150:153], v[204:207], v[110:113]
	v_mfma_f32_16x16x32_bf16 v[106:109], v[172:175], v[204:207], v[106:109]
	v_mfma_f32_16x16x32_bf16 v[94:97], v[150:153], v[212:215], v[94:97]
	v_mfma_f32_16x16x32_bf16 v[90:93], v[172:175], v[212:215], v[90:93]
	v_mfma_f32_16x16x32_bf16 v[78:81], v[150:153], v[220:223], v[78:81]
	v_mfma_f32_16x16x32_bf16 v[74:77], v[172:175], v[220:223], v[74:77]
	v_mfma_f32_16x16x32_bf16 v[118:121], v[176:179], v[192:195], 0
	v_mfma_f32_16x16x32_bf16 v[114:117], v[184:187], v[192:195], 0
	v_mfma_f32_16x16x32_bf16 v[102:105], v[176:179], v[200:203], 0
	v_mfma_f32_16x16x32_bf16 v[98:101], v[184:187], v[200:203], 0
	v_mfma_f32_16x16x32_bf16 v[86:89], v[176:179], v[208:211], 0
	v_mfma_f32_16x16x32_bf16 v[82:85], v[184:187], v[208:211], 0
	v_mfma_f32_16x16x32_bf16 v[70:73], v[176:179], v[216:219], 0
	v_mfma_f32_16x16x32_bf16 v[66:69], v[184:187], v[216:219], 0
	v_mfma_f32_16x16x32_bf16 v[118:121], v[180:183], v[196:199], v[118:121]
	v_mfma_f32_16x16x32_bf16 v[114:117], v[188:191], v[196:199], v[114:117]
	v_mfma_f32_16x16x32_bf16 v[102:105], v[180:183], v[204:207], v[102:105]
	v_mfma_f32_16x16x32_bf16 v[98:101], v[188:191], v[204:207], v[98:101]
	v_mfma_f32_16x16x32_bf16 v[86:89], v[180:183], v[212:215], v[86:89]
	v_mfma_f32_16x16x32_bf16 v[82:85], v[188:191], v[212:215], v[82:85]
	v_mfma_f32_16x16x32_bf16 v[70:73], v[180:183], v[220:223], v[70:73]
	v_mfma_f32_16x16x32_bf16 v[66:69], v[188:191], v[220:223], v[66:69]
	s_cbranch_vccz .Lwb_1129p_0
	s_waitcnt vmcnt(8)
.Lwb_1129p_0:
	s_barrier
	s_add_i32 s0, s48, s40
	v_lshl_add_u64 v[224:225], s[30:31], 0, v[132:133]
	s_mov_b32 m0, s0
	ds_read_b128 v[192:195], v166 offset:16384
	ds_read_b128 v[196:199], v166 offset:17408
	ds_read_b128 v[200:203], v166 offset:18432
	ds_read_b128 v[204:207], v166 offset:19456
	ds_read_b128 v[208:211], v166 offset:20480
	ds_read_b128 v[212:215], v166 offset:21504
	ds_read_b128 v[216:219], v166 offset:22528
	ds_read_b128 v[220:223], v166 offset:23552
	global_load_lds_dwordx4 v[224:225], off
	s_add_i32 m0, s0, 0x2000
	s_add_u32 s0, s30, 0x80000
	v_lshl_add_u64 v[224:225], s[30:31], 0, v[136:137]
	s_addc_u32 s1, s31, 0
	s_add_i32 s2, s49, s40
	global_load_lds_dwordx4 v[224:225], off
	v_lshl_add_u64 v[224:225], s[0:1], 0, v[132:133]
	s_mov_b32 m0, s2
	v_lshl_add_u64 v[226:227], s[34:35], 0, v[134:135]
	global_load_lds_dwordx4 v[224:225], off
	v_lshl_add_u64 v[224:225], s[0:1], 0, v[136:137]
	s_add_i32 m0, s2, 0x2000
	s_nop 0
	global_load_lds_dwordx4 v[224:225], off
	v_lshl_add_u64 v[224:225], s[34:35], 0, v[130:131]
	s_mov_b32 m0, s27
	s_nop 0
	global_load_lds_dwordx4 v[224:225], off
	s_mov_b32 m0, s41
	s_nop 0
	global_load_lds_dwordx4 v[226:227], off
	s_and_b64 vcc, exec, s[14:15]
	s_cbranch_vccnz .Lwa_1129p_1
	s_waitcnt vmcnt(8)
.Lwa_1129p_1:
	s_waitcnt lgkmcnt(0)
	s_barrier
	s_waitcnt lgkmcnt(0)
	v_mfma_f32_16x16x32_bf16 v[62:65], v[146:149], v[192:195], 0
	v_mfma_f32_16x16x32_bf16 v[58:61], v[168:171], v[192:195], 0
	v_mfma_f32_16x16x32_bf16 v[46:49], v[146:149], v[200:203], 0
	v_mfma_f32_16x16x32_bf16 v[42:45], v[168:171], v[200:203], 0
	v_mfma_f32_16x16x32_bf16 v[30:33], v[146:149], v[208:211], 0
	v_mfma_f32_16x16x32_bf16 v[26:29], v[168:171], v[208:211], 0
	v_mfma_f32_16x16x32_bf16 v[14:17], v[146:149], v[216:219], 0
	v_mfma_f32_16x16x32_bf16 v[10:13], v[168:171], v[216:219], 0
	v_mfma_f32_16x16x32_bf16 v[62:65], v[150:153], v[196:199], v[62:65]
	v_mfma_f32_16x16x32_bf16 v[58:61], v[172:175], v[196:199], v[58:61]
	v_mfma_f32_16x16x32_bf16 v[46:49], v[150:153], v[204:207], v[46:49]
	v_mfma_f32_16x16x32_bf16 v[42:45], v[172:175], v[204:207], v[42:45]
	v_mfma_f32_16x16x32_bf16 v[30:33], v[150:153], v[212:215], v[30:33]
	v_mfma_f32_16x16x32_bf16 v[26:29], v[172:175], v[212:215], v[26:29]
	v_mfma_f32_16x16x32_bf16 v[14:17], v[150:153], v[220:223], v[14:17]
	v_mfma_f32_16x16x32_bf16 v[10:13], v[172:175], v[220:223], v[10:13]
	v_mfma_f32_16x16x32_bf16 v[54:57], v[176:179], v[192:195], 0
	v_mfma_f32_16x16x32_bf16 v[50:53], v[184:187], v[192:195], 0
	v_mfma_f32_16x16x32_bf16 v[38:41], v[176:179], v[200:203], 0
	v_mfma_f32_16x16x32_bf16 v[34:37], v[184:187], v[200:203], 0
	v_mfma_f32_16x16x32_bf16 v[22:25], v[176:179], v[208:211], 0
	v_mfma_f32_16x16x32_bf16 v[18:21], v[184:187], v[208:211], 0
	v_mfma_f32_16x16x32_bf16 v[6:9], v[176:179], v[216:219], 0
	v_mfma_f32_16x16x32_bf16 v[2:5], v[184:187], v[216:219], 0
	v_mfma_f32_16x16x32_bf16 v[54:57], v[180:183], v[196:199], v[54:57]
	v_mfma_f32_16x16x32_bf16 v[50:53], v[188:191], v[196:199], v[50:53]
	v_mfma_f32_16x16x32_bf16 v[38:41], v[180:183], v[204:207], v[38:41]
	v_mfma_f32_16x16x32_bf16 v[34:37], v[188:191], v[204:207], v[34:37]
	v_mfma_f32_16x16x32_bf16 v[22:25], v[180:183], v[212:215], v[22:25]
	v_mfma_f32_16x16x32_bf16 v[18:21], v[188:191], v[212:215], v[18:21]
	v_mfma_f32_16x16x32_bf16 v[6:9], v[180:183], v[220:223], v[6:9]
	v_mfma_f32_16x16x32_bf16 v[2:5], v[188:191], v[220:223], v[2:5]
	s_cbranch_vccz .Lwb_1129p_1
	s_waitcnt vmcnt(8)

.Lwa_1129l_0:
	s_waitcnt lgkmcnt(0)
	s_barrier
	s_waitcnt lgkmcnt(0)
	v_mfma_f32_16x16x32_bf16 v[126:129], v[146:149], v[192:195], v[126:129]
	v_mfma_f32_16x16x32_bf16 v[122:125], v[168:171], v[192:195], v[122:125]
	v_mfma_f32_16x16x32_bf16 v[110:113], v[146:149], v[200:203], v[110:113]
	v_mfma_f32_16x16x32_bf16 v[106:109], v[168:171], v[200:203], v[106:109]
	v_mfma_f32_16x16x32_bf16 v[94:97], v[146:149], v[208:211], v[94:97]
	v_mfma_f32_16x16x32_bf16 v[90:93], v[168:171], v[208:211], v[90:93]
	v_mfma_f32_16x16x32_bf16 v[78:81], v[146:149], v[216:219], v[78:81]
	v_mfma_f32_16x16x32_bf16 v[74:77], v[168:171], v[216:219], v[74:77]
	v_mfma_f32_16x16x32_bf16 v[126:129], v[150:153], v[196:199], v[126:129]
	v_mfma_f32_16x16x32_bf16 v[122:125], v[172:175], v[196:199], v[122:125]
	v_mfma_f32_16x16x32_bf16 v[110:113], v[150:153], v[204:207], v[110:113]
	v_mfma_f32_16x16x32_bf16 v[106:109], v[172:175], v[204:207], v[106:109]
	v_mfma_f32_16x16x32_bf16 v[94:97], v[150:153], v[212:215], v[94:97]
	v_mfma_f32_16x16x32_bf16 v[90:93], v[172:175], v[212:215], v[90:93]
	v_mfma_f32_16x16x32_bf16 v[78:81], v[150:153], v[220:223], v[78:81]
	v_mfma_f32_16x16x32_bf16 v[74:77], v[172:175], v[220:223], v[74:77]
	v_mfma_f32_16x16x32_bf16 v[118:121], v[176:179], v[192:195], v[118:121]
	v_mfma_f32_16x16x32_bf16 v[114:117], v[184:187], v[192:195], v[114:117]
	v_mfma_f32_16x16x32_bf16 v[102:105], v[176:179], v[200:203], v[102:105]
	v_mfma_f32_16x16x32_bf16 v[98:101], v[184:187], v[200:203], v[98:101]
	v_mfma_f32_16x16x32_bf16 v[86:89], v[176:179], v[208:211], v[86:89]
	v_mfma_f32_16x16x32_bf16 v[82:85], v[184:187], v[208:211], v[82:85]
	v_mfma_f32_16x16x32_bf16 v[70:73], v[176:179], v[216:219], v[70:73]
	v_mfma_f32_16x16x32_bf16 v[66:69], v[184:187], v[216:219], v[66:69]
	v_mfma_f32_16x16x32_bf16 v[118:121], v[180:183], v[196:199], v[118:121]
	v_mfma_f32_16x16x32_bf16 v[114:117], v[188:191], v[196:199], v[114:117]
	v_mfma_f32_16x16x32_bf16 v[102:105], v[180:183], v[204:207], v[102:105]
	v_mfma_f32_16x16x32_bf16 v[98:101], v[188:191], v[204:207], v[98:101]
	v_mfma_f32_16x16x32_bf16 v[86:89], v[180:183], v[212:215], v[86:89]
	v_mfma_f32_16x16x32_bf16 v[82:85], v[188:191], v[212:215], v[82:85]
	v_mfma_f32_16x16x32_bf16 v[70:73], v[180:183], v[220:223], v[70:73]
	v_mfma_f32_16x16x32_bf16 v[66:69], v[188:191], v[220:223], v[66:69]
	s_cbranch_vccz .Lwb_1129l_0
	s_waitcnt vmcnt(8)

.Lwa_1129l_1:
	s_waitcnt lgkmcnt(0)
	s_barrier
	s_waitcnt lgkmcnt(0)
	v_mfma_f32_16x16x32_bf16 v[62:65], v[146:149], v[192:195], v[62:65]
	v_mfma_f32_16x16x32_bf16 v[58:61], v[168:171], v[192:195], v[58:61]
	v_mfma_f32_16x16x32_bf16 v[46:49], v[146:149], v[200:203], v[46:49]
	v_mfma_f32_16x16x32_bf16 v[42:45], v[168:171], v[200:203], v[42:45]
	v_mfma_f32_16x16x32_bf16 v[30:33], v[146:149], v[208:211], v[30:33]
	v_mfma_f32_16x16x32_bf16 v[26:29], v[168:171], v[208:211], v[26:29]
	v_mfma_f32_16x16x32_bf16 v[14:17], v[146:149], v[216:219], v[14:17]
	v_mfma_f32_16x16x32_bf16 v[10:13], v[168:171], v[216:219], v[10:13]
	v_mfma_f32_16x16x32_bf16 v[62:65], v[150:153], v[196:199], v[62:65]
	v_mfma_f32_16x16x32_bf16 v[58:61], v[172:175], v[196:199], v[58:61]
	v_mfma_f32_16x16x32_bf16 v[46:49], v[150:153], v[204:207], v[46:49]
	v_mfma_f32_16x16x32_bf16 v[42:45], v[172:175], v[204:207], v[42:45]
	v_mfma_f32_16x16x32_bf16 v[30:33], v[150:153], v[212:215], v[30:33]
	v_mfma_f32_16x16x32_bf16 v[26:29], v[172:175], v[212:215], v[26:29]
	v_mfma_f32_16x16x32_bf16 v[14:17], v[150:153], v[220:223], v[14:17]
	v_mfma_f32_16x16x32_bf16 v[10:13], v[172:175], v[220:223], v[10:13]
	v_mfma_f32_16x16x32_bf16 v[54:57], v[176:179], v[192:195], v[54:57]
	v_mfma_f32_16x16x32_bf16 v[50:53], v[184:187], v[192:195], v[50:53]
	v_mfma_f32_16x16x32_bf16 v[38:41], v[176:179], v[200:203], v[38:41]
	v_mfma_f32_16x16x32_bf16 v[34:37], v[184:187], v[200:203], v[34:37]
	v_mfma_f32_16x16x32_bf16 v[22:25], v[176:179], v[208:211], v[22:25]
	v_mfma_f32_16x16x32_bf16 v[18:21], v[184:187], v[208:211], v[18:21]
	v_mfma_f32_16x16x32_bf16 v[6:9], v[176:179], v[216:219], v[6:9]
	v_mfma_f32_16x16x32_bf16 v[2:5], v[184:187], v[216:219], v[2:5]
	v_mfma_f32_16x16x32_bf16 v[54:57], v[180:183], v[196:199], v[54:57]
	v_mfma_f32_16x16x32_bf16 v[50:53], v[188:191], v[196:199], v[50:53]
	v_mfma_f32_16x16x32_bf16 v[38:41], v[180:183], v[204:207], v[38:41]
	v_mfma_f32_16x16x32_bf16 v[34:37], v[188:191], v[204:207], v[34:37]
	v_mfma_f32_16x16x32_bf16 v[22:25], v[180:183], v[212:215], v[22:25]
	v_mfma_f32_16x16x32_bf16 v[18:21], v[188:191], v[212:215], v[18:21]
	v_mfma_f32_16x16x32_bf16 v[6:9], v[180:183], v[220:223], v[6:9]
	v_mfma_f32_16x16x32_bf16 v[2:5], v[188:191], v[220:223], v[2:5]
	s_cbranch_vccz .Lwb_1129l_1
	s_waitcnt vmcnt(8)

.Lwb_1129l_2:
	s_barrier
	s_add_u32 s0, s30, 0x2000
	s_addc_u32 s1, s31, 0
	s_add_i32 s2, s2, s40
	v_lshl_add_u64 v[228:229], s[0:1], 0, v[132:133]
	s_mov_b32 m0, s2
	ds_read_b128 v[192:195], v166 offset:49152
	ds_read_b128 v[196:199], v166 offset:50176
	ds_read_b128 v[200:203], v166 offset:51200
	ds_read_b128 v[204:207], v166 offset:52224
	ds_read_b128 v[208:211], v166 offset:53248
	ds_read_b128 v[212:215], v166 offset:54272
	ds_read_b128 v[216:219], v166 offset:55296
	ds_read_b128 v[220:223], v166 offset:56320
	global_load_lds_dwordx4 v[228:229], off
	s_add_i32 m0, s2, 0x2000
	v_lshl_add_u64 v[228:229], s[0:1], 0, v[136:137]
	s_add_u32 s0, s30, 0x82000
	s_addc_u32 s1, s31, 0
	s_add_i32 s2, s3, s40
	global_load_lds_dwordx4 v[228:229], off
	v_lshl_add_u64 v[228:229], s[0:1], 0, v[132:133]
	s_mov_b32 m0, s2
	v_lshl_add_u64 v[224:225], v[224:225], 0, s[12:13]
	global_load_lds_dwordx4 v[228:229], off
	v_lshl_add_u64 v[228:229], s[0:1], 0, v[136:137]
	s_add_i32 m0, s2, 0x2000
	s_nop 0
	global_load_lds_dwordx4 v[228:229], off
	s_mov_b32 m0, s45
	s_nop 0
	global_load_lds_dwordx4 v[224:225], off
	v_lshl_add_u64 v[224:225], v[226:227], 0, s[12:13]
	s_mov_b32 m0, s46
	s_nop 0
	global_load_lds_dwordx4 v[224:225], off
	s_and_b64 vcc, exec, s[14:15]
	s_cbranch_vccnz .Lwa_1129l_3
	s_waitcnt vmcnt(8)

.Lwb_1129l_3:
	s_barrier
	s_add_i32 s56, s56, 2
	s_add_u32 s54, s54, 0x4000
	s_addc_u32 s55, s55, 0
	s_add_u32 s28, s28, 0x100
	s_addc_u32 s29, s29, 0
	s_cmp_gt_u32 s56, 29
	s_cbranch_scc0 .LBB0_1129
	s_and_b64 vcc, exec, s[14:15]
	s_cbranch_vccz .LBB0_1132
	s_barrier

.Lwa_1153p_0:
	s_waitcnt lgkmcnt(0)
	s_barrier
	s_waitcnt lgkmcnt(0)
	v_mfma_f32_16x16x32_bf16 v[126:129], v[146:149], v[184:187], 0
	v_mfma_f32_16x16x32_bf16 v[122:125], v[160:163], v[184:187], 0
	v_mfma_f32_16x16x32_bf16 v[110:113], v[146:149], v[192:195], 0
	v_mfma_f32_16x16x32_bf16 v[106:109], v[160:163], v[192:195], 0
	v_mfma_f32_16x16x32_bf16 v[94:97], v[146:149], v[200:203], 0
	v_mfma_f32_16x16x32_bf16 v[90:93], v[160:163], v[200:203], 0
	v_mfma_f32_16x16x32_bf16 v[78:81], v[146:149], v[208:211], 0
	v_mfma_f32_16x16x32_bf16 v[74:77], v[160:163], v[208:211], 0
	v_mfma_f32_16x16x32_bf16 v[126:129], v[150:153], v[188:191], v[126:129]
	v_mfma_f32_16x16x32_bf16 v[122:125], v[164:167], v[188:191], v[122:125]
	v_mfma_f32_16x16x32_bf16 v[110:113], v[150:153], v[196:199], v[110:113]
	v_mfma_f32_16x16x32_bf16 v[106:109], v[164:167], v[196:199], v[106:109]
	v_mfma_f32_16x16x32_bf16 v[94:97], v[150:153], v[204:207], v[94:97]
	v_mfma_f32_16x16x32_bf16 v[90:93], v[164:167], v[204:207], v[90:93]
	v_mfma_f32_16x16x32_bf16 v[78:81], v[150:153], v[212:215], v[78:81]
	v_mfma_f32_16x16x32_bf16 v[74:77], v[164:167], v[212:215], v[74:77]
	v_mfma_f32_16x16x32_bf16 v[118:121], v[168:171], v[184:187], 0
	v_mfma_f32_16x16x32_bf16 v[114:117], v[176:179], v[184:187], 0
	v_mfma_f32_16x16x32_bf16 v[102:105], v[168:171], v[192:195], 0
	v_mfma_f32_16x16x32_bf16 v[98:101], v[176:179], v[192:195], 0
	v_mfma_f32_16x16x32_bf16 v[86:89], v[168:171], v[200:203], 0
	v_mfma_f32_16x16x32_bf16 v[82:85], v[176:179], v[200:203], 0
	v_mfma_f32_16x16x32_bf16 v[70:73], v[168:171], v[208:211], 0
	v_mfma_f32_16x16x32_bf16 v[66:69], v[176:179], v[208:211], 0
	v_mfma_f32_16x16x32_bf16 v[118:121], v[172:175], v[188:191], v[118:121]
	v_mfma_f32_16x16x32_bf16 v[114:117], v[180:183], v[188:191], v[114:117]
	v_mfma_f32_16x16x32_bf16 v[102:105], v[172:175], v[196:199], v[102:105]
	v_mfma_f32_16x16x32_bf16 v[98:101], v[180:183], v[196:199], v[98:101]
	v_mfma_f32_16x16x32_bf16 v[86:89], v[172:175], v[204:207], v[86:89]
	v_mfma_f32_16x16x32_bf16 v[82:85], v[180:183], v[204:207], v[82:85]
	v_mfma_f32_16x16x32_bf16 v[70:73], v[172:175], v[212:215], v[70:73]
	v_mfma_f32_16x16x32_bf16 v[66:69], v[180:183], v[212:215], v[66:69]
	s_cbranch_vccz .Lwb_1153p_0
	s_waitcnt vmcnt(8)
.Lwb_1153p_0:
	s_barrier
	s_add_i32 s0, s48, s40
	v_lshl_add_u64 v[216:217], s[30:31], 0, v[132:133]
	s_mov_b32 m0, s0
	ds_read_b128 v[184:187], v155 offset:16384
	ds_read_b128 v[188:191], v155 offset:17408
	ds_read_b128 v[192:195], v155 offset:18432
	ds_read_b128 v[196:199], v155 offset:19456
	ds_read_b128 v[200:203], v155 offset:20480
	ds_read_b128 v[204:207], v155 offset:21504
	ds_read_b128 v[208:211], v155 offset:22528
	ds_read_b128 v[212:215], v155 offset:23552
	global_load_lds_dwordx4 v[216:217], off
	s_add_i32 m0, s0, 0x2000
	s_add_u32 s0, s30, 0x80000
	v_lshl_add_u64 v[216:217], s[30:31], 0, v[136:137]
	s_addc_u32 s1, s31, 0
	s_add_i32 s2, s49, s40
	global_load_lds_dwordx4 v[216:217], off
	v_lshl_add_u64 v[216:217], s[0:1], 0, v[132:133]
	s_mov_b32 m0, s2
	v_lshl_add_u64 v[218:219], s[34:35], 0, v[134:135]
	global_load_lds_dwordx4 v[216:217], off
	v_lshl_add_u64 v[216:217], s[0:1], 0, v[136:137]
	s_add_i32 m0, s2, 0x2000
	s_nop 0
	global_load_lds_dwordx4 v[216:217], off
	v_lshl_add_u64 v[216:217], s[34:35], 0, v[130:131]
	s_mov_b32 m0, s27
	s_nop 0
	global_load_lds_dwordx4 v[216:217], off
	s_mov_b32 m0, s41
	s_nop 0
	global_load_lds_dwordx4 v[218:219], off
	s_and_b64 vcc, exec, s[14:15]
	s_cbranch_vccnz .Lwa_1153p_1
	s_waitcnt vmcnt(8)
.Lwa_1153p_1:
	s_waitcnt lgkmcnt(0)
	s_barrier
	s_waitcnt lgkmcnt(0)
	v_mfma_f32_16x16x32_bf16 v[62:65], v[146:149], v[184:187], 0
	v_mfma_f32_16x16x32_bf16 v[58:61], v[160:163], v[184:187], 0
	v_mfma_f32_16x16x32_bf16 v[46:49], v[146:149], v[192:195], 0
	v_mfma_f32_16x16x32_bf16 v[42:45], v[160:163], v[192:195], 0
	v_mfma_f32_16x16x32_bf16 v[30:33], v[146:149], v[200:203], 0
	v_mfma_f32_16x16x32_bf16 v[26:29], v[160:163], v[200:203], 0
	v_mfma_f32_16x16x32_bf16 v[14:17], v[146:149], v[208:211], 0
	v_mfma_f32_16x16x32_bf16 v[10:13], v[160:163], v[208:211], 0
	v_mfma_f32_16x16x32_bf16 v[62:65], v[150:153], v[188:191], v[62:65]
	v_mfma_f32_16x16x32_bf16 v[58:61], v[164:167], v[188:191], v[58:61]
	v_mfma_f32_16x16x32_bf16 v[46:49], v[150:153], v[196:199], v[46:49]
	v_mfma_f32_16x16x32_bf16 v[42:45], v[164:167], v[196:199], v[42:45]
	v_mfma_f32_16x16x32_bf16 v[30:33], v[150:153], v[204:207], v[30:33]
	v_mfma_f32_16x16x32_bf16 v[26:29], v[164:167], v[204:207], v[26:29]
	v_mfma_f32_16x16x32_bf16 v[14:17], v[150:153], v[212:215], v[14:17]
	v_mfma_f32_16x16x32_bf16 v[10:13], v[164:167], v[212:215], v[10:13]
	v_mfma_f32_16x16x32_bf16 v[54:57], v[168:171], v[184:187], 0
	v_mfma_f32_16x16x32_bf16 v[50:53], v[176:179], v[184:187], 0
	v_mfma_f32_16x16x32_bf16 v[38:41], v[168:171], v[192:195], 0
	v_mfma_f32_16x16x32_bf16 v[34:37], v[176:179], v[192:195], 0
	v_mfma_f32_16x16x32_bf16 v[22:25], v[168:171], v[200:203], 0
	v_mfma_f32_16x16x32_bf16 v[18:21], v[176:179], v[200:203], 0
	v_mfma_f32_16x16x32_bf16 v[6:9], v[168:171], v[208:211], 0
	v_mfma_f32_16x16x32_bf16 v[2:5], v[176:179], v[208:211], 0
	v_mfma_f32_16x16x32_bf16 v[54:57], v[172:175], v[188:191], v[54:57]
	v_mfma_f32_16x16x32_bf16 v[50:53], v[180:183], v[188:191], v[50:53]
	v_mfma_f32_16x16x32_bf16 v[38:41], v[172:175], v[196:199], v[38:41]
	v_mfma_f32_16x16x32_bf16 v[34:37], v[180:183], v[196:199], v[34:37]
	v_mfma_f32_16x16x32_bf16 v[22:25], v[172:175], v[204:207], v[22:25]
	v_mfma_f32_16x16x32_bf16 v[18:21], v[180:183], v[204:207], v[18:21]
	v_mfma_f32_16x16x32_bf16 v[6:9], v[172:175], v[212:215], v[6:9]
	v_mfma_f32_16x16x32_bf16 v[2:5], v[180:183], v[212:215], v[2:5]
	s_cbranch_vccz .Lwb_1153p_1
	s_waitcnt vmcnt(8)

.Lwa_1153l_0:
	s_waitcnt lgkmcnt(0)
	s_barrier
	s_waitcnt lgkmcnt(0)
	v_mfma_f32_16x16x32_bf16 v[126:129], v[146:149], v[184:187], v[126:129]
	v_mfma_f32_16x16x32_bf16 v[122:125], v[160:163], v[184:187], v[122:125]
	v_mfma_f32_16x16x32_bf16 v[110:113], v[146:149], v[192:195], v[110:113]
	v_mfma_f32_16x16x32_bf16 v[106:109], v[160:163], v[192:195], v[106:109]
	v_mfma_f32_16x16x32_bf16 v[94:97], v[146:149], v[200:203], v[94:97]
	v_mfma_f32_16x16x32_bf16 v[90:93], v[160:163], v[200:203], v[90:93]
	v_mfma_f32_16x16x32_bf16 v[78:81], v[146:149], v[208:211], v[78:81]
	v_mfma_f32_16x16x32_bf16 v[74:77], v[160:163], v[208:211], v[74:77]
	v_mfma_f32_16x16x32_bf16 v[126:129], v[150:153], v[188:191], v[126:129]
	v_mfma_f32_16x16x32_bf16 v[122:125], v[164:167], v[188:191], v[122:125]
	v_mfma_f32_16x16x32_bf16 v[110:113], v[150:153], v[196:199], v[110:113]
	v_mfma_f32_16x16x32_bf16 v[106:109], v[164:167], v[196:199], v[106:109]
	v_mfma_f32_16x16x32_bf16 v[94:97], v[150:153], v[204:207], v[94:97]
	v_mfma_f32_16x16x32_bf16 v[90:93], v[164:167], v[204:207], v[90:93]
	v_mfma_f32_16x16x32_bf16 v[78:81], v[150:153], v[212:215], v[78:81]
	v_mfma_f32_16x16x32_bf16 v[74:77], v[164:167], v[212:215], v[74:77]
	v_mfma_f32_16x16x32_bf16 v[118:121], v[168:171], v[184:187], v[118:121]
	v_mfma_f32_16x16x32_bf16 v[114:117], v[176:179], v[184:187], v[114:117]
	v_mfma_f32_16x16x32_bf16 v[102:105], v[168:171], v[192:195], v[102:105]
	v_mfma_f32_16x16x32_bf16 v[98:101], v[176:179], v[192:195], v[98:101]
	v_mfma_f32_16x16x32_bf16 v[86:89], v[168:171], v[200:203], v[86:89]
	v_mfma_f32_16x16x32_bf16 v[82:85], v[176:179], v[200:203], v[82:85]
	v_mfma_f32_16x16x32_bf16 v[70:73], v[168:171], v[208:211], v[70:73]
	v_mfma_f32_16x16x32_bf16 v[66:69], v[176:179], v[208:211], v[66:69]
	v_mfma_f32_16x16x32_bf16 v[118:121], v[172:175], v[188:191], v[118:121]
	v_mfma_f32_16x16x32_bf16 v[114:117], v[180:183], v[188:191], v[114:117]
	v_mfma_f32_16x16x32_bf16 v[102:105], v[172:175], v[196:199], v[102:105]
	v_mfma_f32_16x16x32_bf16 v[98:101], v[180:183], v[196:199], v[98:101]
	v_mfma_f32_16x16x32_bf16 v[86:89], v[172:175], v[204:207], v[86:89]
	v_mfma_f32_16x16x32_bf16 v[82:85], v[180:183], v[204:207], v[82:85]
	v_mfma_f32_16x16x32_bf16 v[70:73], v[172:175], v[212:215], v[70:73]
	v_mfma_f32_16x16x32_bf16 v[66:69], v[180:183], v[212:215], v[66:69]
	s_cbranch_vccz .Lwb_1153l_0
	s_waitcnt vmcnt(8)

.Lwa_1153l_1:
	s_waitcnt lgkmcnt(0)
	s_barrier
	s_waitcnt lgkmcnt(0)
	v_mfma_f32_16x16x32_bf16 v[62:65], v[146:149], v[184:187], v[62:65]
	v_mfma_f32_16x16x32_bf16 v[58:61], v[160:163], v[184:187], v[58:61]
	v_mfma_f32_16x16x32_bf16 v[46:49], v[146:149], v[192:195], v[46:49]
	v_mfma_f32_16x16x32_bf16 v[42:45], v[160:163], v[192:195], v[42:45]
	v_mfma_f32_16x16x32_bf16 v[30:33], v[146:149], v[200:203], v[30:33]
	v_mfma_f32_16x16x32_bf16 v[26:29], v[160:163], v[200:203], v[26:29]
	v_mfma_f32_16x16x32_bf16 v[14:17], v[146:149], v[208:211], v[14:17]
	v_mfma_f32_16x16x32_bf16 v[10:13], v[160:163], v[208:211], v[10:13]
	v_mfma_f32_16x16x32_bf16 v[62:65], v[150:153], v[188:191], v[62:65]
	v_mfma_f32_16x16x32_bf16 v[58:61], v[164:167], v[188:191], v[58:61]
	v_mfma_f32_16x16x32_bf16 v[46:49], v[150:153], v[196:199], v[46:49]
	v_mfma_f32_16x16x32_bf16 v[42:45], v[164:167], v[196:199], v[42:45]
	v_mfma_f32_16x16x32_bf16 v[30:33], v[150:153], v[204:207], v[30:33]
	v_mfma_f32_16x16x32_bf16 v[26:29], v[164:167], v[204:207], v[26:29]
	v_mfma_f32_16x16x32_bf16 v[14:17], v[150:153], v[212:215], v[14:17]
	v_mfma_f32_16x16x32_bf16 v[10:13], v[164:167], v[212:215], v[10:13]
	v_mfma_f32_16x16x32_bf16 v[54:57], v[168:171], v[184:187], v[54:57]
	v_mfma_f32_16x16x32_bf16 v[50:53], v[176:179], v[184:187], v[50:53]
	v_mfma_f32_16x16x32_bf16 v[38:41], v[168:171], v[192:195], v[38:41]
	v_mfma_f32_16x16x32_bf16 v[34:37], v[176:179], v[192:195], v[34:37]
	v_mfma_f32_16x16x32_bf16 v[22:25], v[168:171], v[200:203], v[22:25]
	v_mfma_f32_16x16x32_bf16 v[18:21], v[176:179], v[200:203], v[18:21]
	v_mfma_f32_16x16x32_bf16 v[6:9], v[168:171], v[208:211], v[6:9]
	v_mfma_f32_16x16x32_bf16 v[2:5], v[176:179], v[208:211], v[2:5]
	v_mfma_f32_16x16x32_bf16 v[54:57], v[172:175], v[188:191], v[54:57]
	v_mfma_f32_16x16x32_bf16 v[50:53], v[180:183], v[188:191], v[50:53]
	v_mfma_f32_16x16x32_bf16 v[38:41], v[172:175], v[196:199], v[38:41]
	v_mfma_f32_16x16x32_bf16 v[34:37], v[180:183], v[196:199], v[34:37]
	v_mfma_f32_16x16x32_bf16 v[22:25], v[172:175], v[204:207], v[22:25]
	v_mfma_f32_16x16x32_bf16 v[18:21], v[180:183], v[204:207], v[18:21]
	v_mfma_f32_16x16x32_bf16 v[6:9], v[172:175], v[212:215], v[6:9]
	v_mfma_f32_16x16x32_bf16 v[2:5], v[180:183], v[212:215], v[2:5]
	s_cbranch_vccz .Lwb_1153l_1
	s_waitcnt vmcnt(8)

.Lwb_1153l_2:
	s_barrier
	s_add_u32 s0, s30, 0x2000
	s_addc_u32 s1, s31, 0
	s_add_i32 s2, s2, s40
	v_lshl_add_u64 v[220:221], s[0:1], 0, v[132:133]
	s_mov_b32 m0, s2
	ds_read_b128 v[184:187], v155 offset:49152
	ds_read_b128 v[188:191], v155 offset:50176
	ds_read_b128 v[192:195], v155 offset:51200
	ds_read_b128 v[196:199], v155 offset:52224
	ds_read_b128 v[200:203], v155 offset:53248
	ds_read_b128 v[204:207], v155 offset:54272
	ds_read_b128 v[208:211], v155 offset:55296
	ds_read_b128 v[212:215], v155 offset:56320
	global_load_lds_dwordx4 v[220:221], off
	s_add_i32 m0, s2, 0x2000
	v_lshl_add_u64 v[220:221], s[0:1], 0, v[136:137]
	s_add_u32 s0, s30, 0x82000
	s_addc_u32 s1, s31, 0
	s_add_i32 s2, s3, s40
	global_load_lds_dwordx4 v[220:221], off
	v_lshl_add_u64 v[220:221], s[0:1], 0, v[132:133]
	s_mov_b32 m0, s2
	v_lshl_add_u64 v[216:217], v[216:217], 0, s[12:13]
	global_load_lds_dwordx4 v[220:221], off
	v_lshl_add_u64 v[220:221], s[0:1], 0, v[136:137]
	s_add_i32 m0, s2, 0x2000
	s_nop 0
	global_load_lds_dwordx4 v[220:221], off
	s_mov_b32 m0, s45
	s_nop 0
	global_load_lds_dwordx4 v[216:217], off
	v_lshl_add_u64 v[216:217], v[218:219], 0, s[12:13]
	s_mov_b32 m0, s46
	s_nop 0
	global_load_lds_dwordx4 v[216:217], off
	s_and_b64 vcc, exec, s[14:15]
	s_cbranch_vccnz .Lwa_1153l_3
	s_waitcnt vmcnt(8)

.Lwa_1228p_0:
	s_waitcnt lgkmcnt(0)
	s_barrier
	s_waitcnt lgkmcnt(0)
	v_mfma_f32_16x16x32_bf16 v[126:129], v[146:149], v[186:189], 0
	v_mfma_f32_16x16x32_bf16 v[122:125], v[162:165], v[186:189], 0
	v_mfma_f32_16x16x32_bf16 v[110:113], v[146:149], v[194:197], 0
	v_mfma_f32_16x16x32_bf16 v[106:109], v[162:165], v[194:197], 0
	v_mfma_f32_16x16x32_bf16 v[94:97], v[146:149], v[202:205], 0
	v_mfma_f32_16x16x32_bf16 v[90:93], v[162:165], v[202:205], 0
	v_mfma_f32_16x16x32_bf16 v[78:81], v[146:149], v[210:213], 0
	v_mfma_f32_16x16x32_bf16 v[74:77], v[162:165], v[210:213], 0
	v_mfma_f32_16x16x32_bf16 v[126:129], v[158:161], v[190:193], v[126:129]
	v_mfma_f32_16x16x32_bf16 v[122:125], v[166:169], v[190:193], v[122:125]
	v_mfma_f32_16x16x32_bf16 v[110:113], v[158:161], v[198:201], v[110:113]
	v_mfma_f32_16x16x32_bf16 v[106:109], v[166:169], v[198:201], v[106:109]
	v_mfma_f32_16x16x32_bf16 v[94:97], v[158:161], v[206:209], v[94:97]
	v_mfma_f32_16x16x32_bf16 v[90:93], v[166:169], v[206:209], v[90:93]
	v_mfma_f32_16x16x32_bf16 v[78:81], v[158:161], v[214:217], v[78:81]
	v_mfma_f32_16x16x32_bf16 v[74:77], v[166:169], v[214:217], v[74:77]
	v_mfma_f32_16x16x32_bf16 v[118:121], v[170:173], v[186:189], 0
	v_mfma_f32_16x16x32_bf16 v[114:117], v[178:181], v[186:189], 0
	v_mfma_f32_16x16x32_bf16 v[102:105], v[170:173], v[194:197], 0
	v_mfma_f32_16x16x32_bf16 v[98:101], v[178:181], v[194:197], 0
	v_mfma_f32_16x16x32_bf16 v[86:89], v[170:173], v[202:205], 0
	v_mfma_f32_16x16x32_bf16 v[82:85], v[178:181], v[202:205], 0
	v_mfma_f32_16x16x32_bf16 v[70:73], v[170:173], v[210:213], 0
	v_mfma_f32_16x16x32_bf16 v[66:69], v[178:181], v[210:213], 0
	v_mfma_f32_16x16x32_bf16 v[118:121], v[174:177], v[190:193], v[118:121]
	v_mfma_f32_16x16x32_bf16 v[114:117], v[182:185], v[190:193], v[114:117]
	v_mfma_f32_16x16x32_bf16 v[102:105], v[174:177], v[198:201], v[102:105]
	v_mfma_f32_16x16x32_bf16 v[98:101], v[182:185], v[198:201], v[98:101]
	v_mfma_f32_16x16x32_bf16 v[86:89], v[174:177], v[206:209], v[86:89]
	v_mfma_f32_16x16x32_bf16 v[82:85], v[182:185], v[206:209], v[82:85]
	v_mfma_f32_16x16x32_bf16 v[70:73], v[174:177], v[214:217], v[70:73]
	v_mfma_f32_16x16x32_bf16 v[66:69], v[182:185], v[214:217], v[66:69]
	s_cbranch_vccz .Lwb_1228p_0
	s_waitcnt vmcnt(8)
.Lwb_1228p_0:
	s_barrier
	s_add_i32 s0, s54, s46
	v_lshl_add_u64 v[150:151], s[38:39], 0, v[132:133]
	s_mov_b32 m0, s0
	ds_read_b128 v[186:189], v156 offset:16384
	ds_read_b128 v[190:193], v156 offset:17408
	ds_read_b128 v[194:197], v156 offset:18432
	ds_read_b128 v[198:201], v156 offset:19456
	ds_read_b128 v[202:205], v156 offset:20480
	ds_read_b128 v[206:209], v156 offset:21504
	ds_read_b128 v[210:213], v156 offset:22528
	ds_read_b128 v[214:217], v156 offset:23552
	global_load_lds_dwordx4 v[150:151], off
	s_add_i32 m0, s0, 0x2000
	s_add_u32 s0, s38, 0x80000
	v_lshl_add_u64 v[150:151], s[38:39], 0, v[136:137]
	s_addc_u32 s1, s39, 0
	s_add_i32 s2, s55, s46
	global_load_lds_dwordx4 v[150:151], off
	v_lshl_add_u64 v[150:151], s[0:1], 0, v[132:133]
	s_mov_b32 m0, s2
	v_lshl_add_u64 v[218:219], s[40:41], 0, v[134:135]
	global_load_lds_dwordx4 v[150:151], off
	v_lshl_add_u64 v[150:151], s[0:1], 0, v[136:137]
	s_add_i32 m0, s2, 0x2000
	s_nop 0
	global_load_lds_dwordx4 v[150:151], off
	v_lshl_add_u64 v[150:151], s[40:41], 0, v[130:131]
	s_mov_b32 m0, s35
	s_nop 0
	global_load_lds_dwordx4 v[150:151], off
	s_mov_b32 m0, s47
	s_nop 0
	global_load_lds_dwordx4 v[218:219], off
	s_and_b64 vcc, exec, s[14:15]
	s_cbranch_vccnz .Lwa_1228p_1
	s_waitcnt vmcnt(8)
.Lwa_1228p_1:
	s_waitcnt lgkmcnt(0)
	s_barrier
	s_waitcnt lgkmcnt(0)
	v_mfma_f32_16x16x32_bf16 v[62:65], v[146:149], v[186:189], 0
	v_mfma_f32_16x16x32_bf16 v[58:61], v[162:165], v[186:189], 0
	v_mfma_f32_16x16x32_bf16 v[46:49], v[146:149], v[194:197], 0
	v_mfma_f32_16x16x32_bf16 v[42:45], v[162:165], v[194:197], 0
	v_mfma_f32_16x16x32_bf16 v[30:33], v[146:149], v[202:205], 0
	v_mfma_f32_16x16x32_bf16 v[26:29], v[162:165], v[202:205], 0
	v_mfma_f32_16x16x32_bf16 v[14:17], v[146:149], v[210:213], 0
	v_mfma_f32_16x16x32_bf16 v[10:13], v[162:165], v[210:213], 0
	v_mfma_f32_16x16x32_bf16 v[62:65], v[158:161], v[190:193], v[62:65]
	v_mfma_f32_16x16x32_bf16 v[58:61], v[166:169], v[190:193], v[58:61]
	v_mfma_f32_16x16x32_bf16 v[46:49], v[158:161], v[198:201], v[46:49]
	v_mfma_f32_16x16x32_bf16 v[42:45], v[166:169], v[198:201], v[42:45]
	v_mfma_f32_16x16x32_bf16 v[30:33], v[158:161], v[206:209], v[30:33]
	v_mfma_f32_16x16x32_bf16 v[26:29], v[166:169], v[206:209], v[26:29]
	v_mfma_f32_16x16x32_bf16 v[14:17], v[158:161], v[214:217], v[14:17]
	v_mfma_f32_16x16x32_bf16 v[10:13], v[166:169], v[214:217], v[10:13]
	v_mfma_f32_16x16x32_bf16 v[54:57], v[170:173], v[186:189], 0
	v_mfma_f32_16x16x32_bf16 v[50:53], v[178:181], v[186:189], 0
	v_mfma_f32_16x16x32_bf16 v[38:41], v[170:173], v[194:197], 0
	v_mfma_f32_16x16x32_bf16 v[34:37], v[178:181], v[194:197], 0
	v_mfma_f32_16x16x32_bf16 v[22:25], v[170:173], v[202:205], 0
	v_mfma_f32_16x16x32_bf16 v[18:21], v[178:181], v[202:205], 0
	v_mfma_f32_16x16x32_bf16 v[6:9], v[170:173], v[210:213], 0
	v_mfma_f32_16x16x32_bf16 v[2:5], v[178:181], v[210:213], 0
	v_mfma_f32_16x16x32_bf16 v[54:57], v[174:177], v[190:193], v[54:57]
	v_mfma_f32_16x16x32_bf16 v[50:53], v[182:185], v[190:193], v[50:53]
	v_mfma_f32_16x16x32_bf16 v[38:41], v[174:177], v[198:201], v[38:41]
	v_mfma_f32_16x16x32_bf16 v[34:37], v[182:185], v[198:201], v[34:37]
	v_mfma_f32_16x16x32_bf16 v[22:25], v[174:177], v[206:209], v[22:25]
	v_mfma_f32_16x16x32_bf16 v[18:21], v[182:185], v[206:209], v[18:21]
	v_mfma_f32_16x16x32_bf16 v[6:9], v[174:177], v[214:217], v[6:9]
	v_mfma_f32_16x16x32_bf16 v[2:5], v[182:185], v[214:217], v[2:5]
	s_cbranch_vccz .Lwb_1228p_1
	s_waitcnt vmcnt(8)

.Lwa_1228l_0:
	s_waitcnt lgkmcnt(0)
	s_barrier
	s_waitcnt lgkmcnt(0)
	v_mfma_f32_16x16x32_bf16 v[126:129], v[146:149], v[186:189], v[126:129]
	v_mfma_f32_16x16x32_bf16 v[122:125], v[162:165], v[186:189], v[122:125]
	v_mfma_f32_16x16x32_bf16 v[110:113], v[146:149], v[194:197], v[110:113]
	v_mfma_f32_16x16x32_bf16 v[106:109], v[162:165], v[194:197], v[106:109]
	v_mfma_f32_16x16x32_bf16 v[94:97], v[146:149], v[202:205], v[94:97]
	v_mfma_f32_16x16x32_bf16 v[90:93], v[162:165], v[202:205], v[90:93]
	v_mfma_f32_16x16x32_bf16 v[78:81], v[146:149], v[210:213], v[78:81]
	v_mfma_f32_16x16x32_bf16 v[74:77], v[162:165], v[210:213], v[74:77]
	v_mfma_f32_16x16x32_bf16 v[126:129], v[158:161], v[190:193], v[126:129]
	v_mfma_f32_16x16x32_bf16 v[122:125], v[166:169], v[190:193], v[122:125]
	v_mfma_f32_16x16x32_bf16 v[110:113], v[158:161], v[198:201], v[110:113]
	v_mfma_f32_16x16x32_bf16 v[106:109], v[166:169], v[198:201], v[106:109]
	v_mfma_f32_16x16x32_bf16 v[94:97], v[158:161], v[206:209], v[94:97]
	v_mfma_f32_16x16x32_bf16 v[90:93], v[166:169], v[206:209], v[90:93]
	v_mfma_f32_16x16x32_bf16 v[78:81], v[158:161], v[214:217], v[78:81]
	v_mfma_f32_16x16x32_bf16 v[74:77], v[166:169], v[214:217], v[74:77]
	v_mfma_f32_16x16x32_bf16 v[118:121], v[170:173], v[186:189], v[118:121]
	v_mfma_f32_16x16x32_bf16 v[114:117], v[178:181], v[186:189], v[114:117]
	v_mfma_f32_16x16x32_bf16 v[102:105], v[170:173], v[194:197], v[102:105]
	v_mfma_f32_16x16x32_bf16 v[98:101], v[178:181], v[194:197], v[98:101]
	v_mfma_f32_16x16x32_bf16 v[86:89], v[170:173], v[202:205], v[86:89]
	v_mfma_f32_16x16x32_bf16 v[82:85], v[178:181], v[202:205], v[82:85]
	v_mfma_f32_16x16x32_bf16 v[70:73], v[170:173], v[210:213], v[70:73]
	v_mfma_f32_16x16x32_bf16 v[66:69], v[178:181], v[210:213], v[66:69]
	v_mfma_f32_16x16x32_bf16 v[118:121], v[174:177], v[190:193], v[118:121]
	v_mfma_f32_16x16x32_bf16 v[114:117], v[182:185], v[190:193], v[114:117]
	v_mfma_f32_16x16x32_bf16 v[102:105], v[174:177], v[198:201], v[102:105]
	v_mfma_f32_16x16x32_bf16 v[98:101], v[182:185], v[198:201], v[98:101]
	v_mfma_f32_16x16x32_bf16 v[86:89], v[174:177], v[206:209], v[86:89]
	v_mfma_f32_16x16x32_bf16 v[82:85], v[182:185], v[206:209], v[82:85]
	v_mfma_f32_16x16x32_bf16 v[70:73], v[174:177], v[214:217], v[70:73]
	v_mfma_f32_16x16x32_bf16 v[66:69], v[182:185], v[214:217], v[66:69]
	s_cbranch_vccz .Lwb_1228l_0
	s_waitcnt vmcnt(8)

.Lwa_1228l_1:
	s_waitcnt lgkmcnt(0)
	s_barrier
	s_waitcnt lgkmcnt(0)
	v_mfma_f32_16x16x32_bf16 v[62:65], v[146:149], v[186:189], v[62:65]
	v_mfma_f32_16x16x32_bf16 v[58:61], v[162:165], v[186:189], v[58:61]
	v_mfma_f32_16x16x32_bf16 v[46:49], v[146:149], v[194:197], v[46:49]
	v_mfma_f32_16x16x32_bf16 v[42:45], v[162:165], v[194:197], v[42:45]
	v_mfma_f32_16x16x32_bf16 v[30:33], v[146:149], v[202:205], v[30:33]
	v_mfma_f32_16x16x32_bf16 v[26:29], v[162:165], v[202:205], v[26:29]
	v_mfma_f32_16x16x32_bf16 v[14:17], v[146:149], v[210:213], v[14:17]
	v_mfma_f32_16x16x32_bf16 v[10:13], v[162:165], v[210:213], v[10:13]
	v_mfma_f32_16x16x32_bf16 v[62:65], v[158:161], v[190:193], v[62:65]
	v_mfma_f32_16x16x32_bf16 v[58:61], v[166:169], v[190:193], v[58:61]
	v_mfma_f32_16x16x32_bf16 v[46:49], v[158:161], v[198:201], v[46:49]
	v_mfma_f32_16x16x32_bf16 v[42:45], v[166:169], v[198:201], v[42:45]
	v_mfma_f32_16x16x32_bf16 v[30:33], v[158:161], v[206:209], v[30:33]
	v_mfma_f32_16x16x32_bf16 v[26:29], v[166:169], v[206:209], v[26:29]
	v_mfma_f32_16x16x32_bf16 v[14:17], v[158:161], v[214:217], v[14:17]
	v_mfma_f32_16x16x32_bf16 v[10:13], v[166:169], v[214:217], v[10:13]
	v_mfma_f32_16x16x32_bf16 v[54:57], v[170:173], v[186:189], v[54:57]
	v_mfma_f32_16x16x32_bf16 v[50:53], v[178:181], v[186:189], v[50:53]
	v_mfma_f32_16x16x32_bf16 v[38:41], v[170:173], v[194:197], v[38:41]
	v_mfma_f32_16x16x32_bf16 v[34:37], v[178:181], v[194:197], v[34:37]
	v_mfma_f32_16x16x32_bf16 v[22:25], v[170:173], v[202:205], v[22:25]
	v_mfma_f32_16x16x32_bf16 v[18:21], v[178:181], v[202:205], v[18:21]
	v_mfma_f32_16x16x32_bf16 v[6:9], v[170:173], v[210:213], v[6:9]
	v_mfma_f32_16x16x32_bf16 v[2:5], v[178:181], v[210:213], v[2:5]
	v_mfma_f32_16x16x32_bf16 v[54:57], v[174:177], v[190:193], v[54:57]
	v_mfma_f32_16x16x32_bf16 v[50:53], v[182:185], v[190:193], v[50:53]
	v_mfma_f32_16x16x32_bf16 v[38:41], v[174:177], v[198:201], v[38:41]
	v_mfma_f32_16x16x32_bf16 v[34:37], v[182:185], v[198:201], v[34:37]
	v_mfma_f32_16x16x32_bf16 v[22:25], v[174:177], v[206:209], v[22:25]
	v_mfma_f32_16x16x32_bf16 v[18:21], v[182:185], v[206:209], v[18:21]
	v_mfma_f32_16x16x32_bf16 v[6:9], v[174:177], v[214:217], v[6:9]
	v_mfma_f32_16x16x32_bf16 v[2:5], v[182:185], v[214:217], v[2:5]
	s_cbranch_vccz .Lwb_1228l_1
	s_waitcnt vmcnt(8)

.Lwb_1228l_2:
	s_barrier
	s_add_u32 s0, s38, 0x2000
	s_addc_u32 s1, s39, 0
	s_add_i32 s2, s2, s46
	v_lshl_add_u64 v[220:221], s[0:1], 0, v[132:133]
	s_mov_b32 m0, s2
	ds_read_b128 v[186:189], v156 offset:49152
	ds_read_b128 v[190:193], v156 offset:50176
	ds_read_b128 v[194:197], v156 offset:51200
	ds_read_b128 v[198:201], v156 offset:52224
	ds_read_b128 v[202:205], v156 offset:53248
	ds_read_b128 v[206:209], v156 offset:54272
	ds_read_b128 v[210:213], v156 offset:55296
	ds_read_b128 v[214:217], v156 offset:56320
	global_load_lds_dwordx4 v[220:221], off
	s_add_i32 m0, s2, 0x2000
	v_lshl_add_u64 v[220:221], s[0:1], 0, v[136:137]
	s_add_u32 s0, s38, 0x82000
	s_addc_u32 s1, s39, 0
	s_add_i32 s2, s3, s46
	global_load_lds_dwordx4 v[220:221], off
	v_lshl_add_u64 v[220:221], s[0:1], 0, v[132:133]
	s_mov_b32 m0, s2
	v_lshl_add_u64 v[150:151], v[150:151], 0, s[12:13]
	global_load_lds_dwordx4 v[220:221], off
	v_lshl_add_u64 v[220:221], s[0:1], 0, v[136:137]
	s_add_i32 m0, s2, 0x2000
	s_nop 0
	global_load_lds_dwordx4 v[220:221], off
	s_mov_b32 m0, s51
	s_nop 0
	global_load_lds_dwordx4 v[150:151], off
	v_lshl_add_u64 v[150:151], v[218:219], 0, s[12:13]
	s_mov_b32 m0, s52
	s_nop 0
	global_load_lds_dwordx4 v[150:151], off
	s_and_b64 vcc, exec, s[14:15]
	s_cbranch_vccnz .Lwa_1228l_3
	s_waitcnt vmcnt(8)

.Lwb_1228l_3:
	s_barrier
	s_add_i32 s61, s61, 2
	s_add_u32 s59, s59, 0x4000
	s_addc_u32 s60, s60, 0
	s_add_u32 s36, s36, 0x100
	s_addc_u32 s37, s37, 0
	s_cmp_gt_u32 s61, 29
	s_cbranch_scc0 .LBB0_1228
	s_and_b64 vcc, exec, s[14:15]
	s_cbranch_vccz .LBB0_1231
	s_barrier

.LBB0_1481:
	s_lshl_b32 s1, s30, 7
	s_ashr_i32 s0, s30, 4
	s_and_b32 s1, s1, 0x780
	v_or_b32_e32 v240, s1, v184
	s_ashr_i32 s1, s0, 31
	s_lshl_b64 s[0:1], s[0:1], 13
	s_add_u32 s2, s8, s0
	s_addc_u32 s3, s9, s1
	v_lshlrev_b32_e32 v240, 2, v240
	s_add_u32 s0, s10, s0
	s_addc_u32 s1, s11, s1
	global_load_dwordx4 v[224:227], v240, s[2:3]
	global_load_dwordx4 v[228:231], v240, s[2:3] offset:16
	global_load_dwordx4 v[232:235], v240, s[0:1]
	global_load_dwordx4 v[236:239], v240, s[0:1] offset:16
	s_ashr_i32 s21, s20, 31
	s_lshl_b64 s[0:1], s[20:21], 19
	s_add_u32 s24, s47, s0
	s_addc_u32 s25, s48, s1
	s_and_b64 s[0:1], s[4:5], exec
	s_cselect_b32 s21, s25, s37
	s_cselect_b32 s63, s24, s36
	s_ashr_i32 s23, s22, 31
	s_lshl_b64 s[0:1], s[22:23], 19
	s_add_u32 s26, s45, s0
	s_addc_u32 s27, s46, s1
	s_and_b64 s[0:1], s[4:5], exec
	s_cselect_b32 s23, s27, s35
	s_cselect_b32 s64, s26, s34
	s_add_u32 s65, s34, 0x4000
	s_addc_u32 s66, s35, 0
	s_add_u32 s34, s36, 0x40080
	s_addc_u32 s35, s37, 0
	s_mov_b32 s67, -2
	ds_read_b128 v[26:29], v185
	ds_read_b128 v[30:33], v185 offset:1024
	ds_read_b128 v[18:21], v185 offset:2048
	ds_read_b128 v[22:25], v185 offset:3072
	ds_read_b128 v[10:13], v186
	ds_read_b128 v[14:17], v186 offset:1024
	ds_read_b128 v[2:5], v186 offset:2048
	ds_read_b128 v[6:9], v186 offset:3072
	s_add_u32 s0, s34, 0xfffc0080
	s_addc_u32 s1, s35, -1
	s_cmp_eq_u32 s67, 12
	s_cselect_b32 s39, s21, s1
	s_cselect_b32 s38, s63, s0
	s_cselect_b32 s37, s23, s66
	s_cselect_b32 s36, s64, s65
	v_lshl_add_u64 v[178:179], s[34:35], 0, v[172:173]
	s_add_i32 m0, s29, 0xc000
	ds_read_b128 v[190:193], v187
	ds_read_b128 v[194:197], v187 offset:1024
	ds_read_b128 v[198:201], v187 offset:2048
	ds_read_b128 v[202:205], v187 offset:3072
	ds_read_b128 v[206:209], v187 offset:4096
	ds_read_b128 v[210:213], v187 offset:5120
	ds_read_b128 v[214:217], v187 offset:6144
	ds_read_b128 v[218:221], v187 offset:7168
	global_load_lds_dwordx4 v[178:179], off
	v_lshl_add_u64 v[178:179], s[34:35], 0, v[174:175]
	s_add_i32 m0, s29, 0xe000
	s_nop 0
	global_load_lds_dwordx4 v[178:179], off
	s_waitcnt vmcnt(8)
	s_waitcnt lgkmcnt(0)
	s_barrier
	s_waitcnt lgkmcnt(0)
	v_mfma_scale_f32_16x16x128_f8f6f4 v[158:161], v[26:33], v[190:197], 0, v188, v188 op_sel_hi:[0,0,0]
	v_mfma_scale_f32_16x16x128_f8f6f4 v[154:157], v[18:25], v[190:197], 0, v188, v188 op_sel_hi:[0,0,0]
	v_mfma_scale_f32_16x16x128_f8f6f4 v[142:145], v[26:33], v[198:205], 0, v188, v188 op_sel_hi:[0,0,0]
	v_mfma_scale_f32_16x16x128_f8f6f4 v[138:141], v[18:25], v[198:205], 0, v188, v188 op_sel_hi:[0,0,0]
	v_mfma_scale_f32_16x16x128_f8f6f4 v[126:129], v[26:33], v[206:213], 0, v188, v188 op_sel_hi:[0,0,0]
	v_mfma_scale_f32_16x16x128_f8f6f4 v[122:125], v[18:25], v[206:213], 0, v188, v188 op_sel_hi:[0,0,0]
	v_mfma_scale_f32_16x16x128_f8f6f4 v[110:113], v[26:33], v[214:221], 0, v188, v188 op_sel_hi:[0,0,0]
	v_mfma_scale_f32_16x16x128_f8f6f4 v[106:109], v[18:25], v[214:221], 0, v188, v188 op_sel_hi:[0,0,0]
	v_mfma_scale_f32_16x16x128_f8f6f4 v[150:153], v[10:17], v[190:197], 0, v188, v188 op_sel_hi:[0,0,0]
	v_mfma_scale_f32_16x16x128_f8f6f4 v[146:149], v[2:9], v[190:197], 0, v188, v188 op_sel_hi:[0,0,0]
	v_mfma_scale_f32_16x16x128_f8f6f4 v[134:137], v[10:17], v[198:205], 0, v188, v188 op_sel_hi:[0,0,0]
	v_mfma_scale_f32_16x16x128_f8f6f4 v[130:133], v[2:9], v[198:205], 0, v188, v188 op_sel_hi:[0,0,0]
	v_mfma_scale_f32_16x16x128_f8f6f4 v[118:121], v[10:17], v[206:213], 0, v188, v188 op_sel_hi:[0,0,0]
	v_mfma_scale_f32_16x16x128_f8f6f4 v[114:117], v[2:9], v[206:213], 0, v188, v188 op_sel_hi:[0,0,0]
	v_mfma_scale_f32_16x16x128_f8f6f4 v[102:105], v[10:17], v[214:221], 0, v188, v188 op_sel_hi:[0,0,0]
	v_mfma_scale_f32_16x16x128_f8f6f4 v[98:101], v[2:9], v[214:221], 0, v188, v188 op_sel_hi:[0,0,0]
	s_barrier
	s_add_i32 s0, s57, s49
	v_lshl_add_u64 v[178:179], s[36:37], 0, v[164:165]
	s_mov_b32 m0, s0
	ds_read_b128 v[190:193], v187 offset:16384
	ds_read_b128 v[194:197], v187 offset:17408
	ds_read_b128 v[198:201], v187 offset:18432
	ds_read_b128 v[202:205], v187 offset:19456
	ds_read_b128 v[206:209], v187 offset:20480
	ds_read_b128 v[210:213], v187 offset:21504
	ds_read_b128 v[214:217], v187 offset:22528
	ds_read_b128 v[218:221], v187 offset:23552
	global_load_lds_dwordx4 v[178:179], off
	s_add_i32 m0, s0, 0x2000
	s_add_u32 s0, s36, 0x40000
	v_lshl_add_u64 v[178:179], s[36:37], 0, v[168:169]
	s_addc_u32 s1, s37, 0
	s_add_i32 s2, s58, s49
	global_load_lds_dwordx4 v[178:179], off
	v_lshl_add_u64 v[178:179], s[0:1], 0, v[164:165]
	s_mov_b32 m0, s2
	v_lshl_add_u64 v[180:181], s[38:39], 0, v[166:167]
	global_load_lds_dwordx4 v[178:179], off
	v_lshl_add_u64 v[178:179], s[0:1], 0, v[168:169]
	s_add_i32 m0, s2, 0x2000
	s_nop 0
	global_load_lds_dwordx4 v[178:179], off
	v_lshl_add_u64 v[178:179], s[38:39], 0, v[162:163]
	s_mov_b32 m0, s29
	s_nop 0
	global_load_lds_dwordx4 v[178:179], off
	s_mov_b32 m0, s31
	s_nop 0
	global_load_lds_dwordx4 v[180:181], off
	s_waitcnt vmcnt(8)
	s_waitcnt lgkmcnt(0)
	s_barrier
	s_waitcnt lgkmcnt(0)
	v_mfma_scale_f32_16x16x128_f8f6f4 v[94:97], v[26:33], v[190:197], 0, v188, v188 op_sel_hi:[0,0,0]
	v_mfma_scale_f32_16x16x128_f8f6f4 v[90:93], v[18:25], v[190:197], 0, v188, v188 op_sel_hi:[0,0,0]
	v_mfma_scale_f32_16x16x128_f8f6f4 v[78:81], v[26:33], v[198:205], 0, v188, v188 op_sel_hi:[0,0,0]
	v_mfma_scale_f32_16x16x128_f8f6f4 v[74:77], v[18:25], v[198:205], 0, v188, v188 op_sel_hi:[0,0,0]
	v_mfma_scale_f32_16x16x128_f8f6f4 v[62:65], v[26:33], v[206:213], 0, v188, v188 op_sel_hi:[0,0,0]
	v_mfma_scale_f32_16x16x128_f8f6f4 v[58:61], v[18:25], v[206:213], 0, v188, v188 op_sel_hi:[0,0,0]
	v_mfma_scale_f32_16x16x128_f8f6f4 v[46:49], v[26:33], v[214:221], 0, v188, v188 op_sel_hi:[0,0,0]
	v_mfma_scale_f32_16x16x128_f8f6f4 v[42:45], v[18:25], v[214:221], 0, v188, v188 op_sel_hi:[0,0,0]
	v_mfma_scale_f32_16x16x128_f8f6f4 v[86:89], v[10:17], v[190:197], 0, v188, v188 op_sel_hi:[0,0,0]
	v_mfma_scale_f32_16x16x128_f8f6f4 v[82:85], v[2:9], v[190:197], 0, v188, v188 op_sel_hi:[0,0,0]
	v_mfma_scale_f32_16x16x128_f8f6f4 v[70:73], v[10:17], v[198:205], 0, v188, v188 op_sel_hi:[0,0,0]
	v_mfma_scale_f32_16x16x128_f8f6f4 v[66:69], v[2:9], v[198:205], 0, v188, v188 op_sel_hi:[0,0,0]
	v_mfma_scale_f32_16x16x128_f8f6f4 v[54:57], v[10:17], v[206:213], 0, v188, v188 op_sel_hi:[0,0,0]
	v_mfma_scale_f32_16x16x128_f8f6f4 v[50:53], v[2:9], v[206:213], 0, v188, v188 op_sel_hi:[0,0,0]
	v_mfma_scale_f32_16x16x128_f8f6f4 v[38:41], v[10:17], v[214:221], 0, v188, v188 op_sel_hi:[0,0,0]
	v_mfma_scale_f32_16x16x128_f8f6f4 v[34:37], v[2:9], v[214:221], 0, v188, v188 op_sel_hi:[0,0,0]
	s_barrier
	s_branch .Lmid_1482
.LBB0_1482:
	ds_read_b128 v[26:29], v185
	ds_read_b128 v[30:33], v185 offset:1024
	ds_read_b128 v[18:21], v185 offset:2048
	ds_read_b128 v[22:25], v185 offset:3072
	ds_read_b128 v[10:13], v186
	ds_read_b128 v[14:17], v186 offset:1024
	ds_read_b128 v[2:5], v186 offset:2048
	ds_read_b128 v[6:9], v186 offset:3072
	s_add_u32 s0, s34, 0xfffc0080
	s_addc_u32 s1, s35, -1
	s_cmp_eq_u32 s67, 12
	s_cselect_b32 s39, s21, s1
	s_cselect_b32 s38, s63, s0
	s_cselect_b32 s37, s23, s66
	s_cselect_b32 s36, s64, s65
	v_lshl_add_u64 v[178:179], s[34:35], 0, v[172:173]
	s_add_i32 m0, s29, 0xc000
	ds_read_b128 v[190:193], v187
	ds_read_b128 v[194:197], v187 offset:1024
	ds_read_b128 v[198:201], v187 offset:2048
	ds_read_b128 v[202:205], v187 offset:3072
	ds_read_b128 v[206:209], v187 offset:4096
	ds_read_b128 v[210:213], v187 offset:5120
	ds_read_b128 v[214:217], v187 offset:6144
	ds_read_b128 v[218:221], v187 offset:7168
	global_load_lds_dwordx4 v[178:179], off
	v_lshl_add_u64 v[178:179], s[34:35], 0, v[174:175]
	s_add_i32 m0, s29, 0xe000
	s_nop 0
	global_load_lds_dwordx4 v[178:179], off
	s_waitcnt vmcnt(8)
	s_waitcnt lgkmcnt(0)
	s_barrier
	s_waitcnt lgkmcnt(0)
	v_mfma_scale_f32_16x16x128_f8f6f4 v[158:161], v[26:33], v[190:197], v[158:161], v188, v188 op_sel_hi:[0,0,0]
	v_mfma_scale_f32_16x16x128_f8f6f4 v[154:157], v[18:25], v[190:197], v[154:157], v188, v188 op_sel_hi:[0,0,0]
	v_mfma_scale_f32_16x16x128_f8f6f4 v[142:145], v[26:33], v[198:205], v[142:145], v188, v188 op_sel_hi:[0,0,0]
	v_mfma_scale_f32_16x16x128_f8f6f4 v[138:141], v[18:25], v[198:205], v[138:141], v188, v188 op_sel_hi:[0,0,0]
	v_mfma_scale_f32_16x16x128_f8f6f4 v[126:129], v[26:33], v[206:213], v[126:129], v188, v188 op_sel_hi:[0,0,0]
	v_mfma_scale_f32_16x16x128_f8f6f4 v[122:125], v[18:25], v[206:213], v[122:125], v188, v188 op_sel_hi:[0,0,0]
	v_mfma_scale_f32_16x16x128_f8f6f4 v[110:113], v[26:33], v[214:221], v[110:113], v188, v188 op_sel_hi:[0,0,0]
	v_mfma_scale_f32_16x16x128_f8f6f4 v[106:109], v[18:25], v[214:221], v[106:109], v188, v188 op_sel_hi:[0,0,0]
	v_mfma_scale_f32_16x16x128_f8f6f4 v[150:153], v[10:17], v[190:197], v[150:153], v188, v188 op_sel_hi:[0,0,0]
	v_mfma_scale_f32_16x16x128_f8f6f4 v[146:149], v[2:9], v[190:197], v[146:149], v188, v188 op_sel_hi:[0,0,0]
	v_mfma_scale_f32_16x16x128_f8f6f4 v[134:137], v[10:17], v[198:205], v[134:137], v188, v188 op_sel_hi:[0,0,0]
	v_mfma_scale_f32_16x16x128_f8f6f4 v[130:133], v[2:9], v[198:205], v[130:133], v188, v188 op_sel_hi:[0,0,0]
	v_mfma_scale_f32_16x16x128_f8f6f4 v[118:121], v[10:17], v[206:213], v[118:121], v188, v188 op_sel_hi:[0,0,0]
	v_mfma_scale_f32_16x16x128_f8f6f4 v[114:117], v[2:9], v[206:213], v[114:117], v188, v188 op_sel_hi:[0,0,0]
	v_mfma_scale_f32_16x16x128_f8f6f4 v[102:105], v[10:17], v[214:221], v[102:105], v188, v188 op_sel_hi:[0,0,0]
	v_mfma_scale_f32_16x16x128_f8f6f4 v[98:101], v[2:9], v[214:221], v[98:101], v188, v188 op_sel_hi:[0,0,0]
	s_barrier
	s_add_i32 s0, s57, s49
	v_lshl_add_u64 v[178:179], s[36:37], 0, v[164:165]
	s_mov_b32 m0, s0
	ds_read_b128 v[190:193], v187 offset:16384
	ds_read_b128 v[194:197], v187 offset:17408
	ds_read_b128 v[198:201], v187 offset:18432
	ds_read_b128 v[202:205], v187 offset:19456
	ds_read_b128 v[206:209], v187 offset:20480
	ds_read_b128 v[210:213], v187 offset:21504
	ds_read_b128 v[214:217], v187 offset:22528
	ds_read_b128 v[218:221], v187 offset:23552
	global_load_lds_dwordx4 v[178:179], off
	s_add_i32 m0, s0, 0x2000
	s_add_u32 s0, s36, 0x40000
	v_lshl_add_u64 v[178:179], s[36:37], 0, v[168:169]
	s_addc_u32 s1, s37, 0
	s_add_i32 s2, s58, s49
	global_load_lds_dwordx4 v[178:179], off
	v_lshl_add_u64 v[178:179], s[0:1], 0, v[164:165]
	s_mov_b32 m0, s2
	v_lshl_add_u64 v[180:181], s[38:39], 0, v[166:167]
	global_load_lds_dwordx4 v[178:179], off
	v_lshl_add_u64 v[178:179], s[0:1], 0, v[168:169]
	s_add_i32 m0, s2, 0x2000
	s_nop 0
	global_load_lds_dwordx4 v[178:179], off
	v_lshl_add_u64 v[178:179], s[38:39], 0, v[162:163]
	s_mov_b32 m0, s29
	s_nop 0
	global_load_lds_dwordx4 v[178:179], off
	s_mov_b32 m0, s31
	s_nop 0
	global_load_lds_dwordx4 v[180:181], off
	s_waitcnt vmcnt(8)
	s_waitcnt lgkmcnt(0)
	s_barrier
	s_waitcnt lgkmcnt(0)
	v_mfma_scale_f32_16x16x128_f8f6f4 v[94:97], v[26:33], v[190:197], v[94:97], v188, v188 op_sel_hi:[0,0,0]
	v_mfma_scale_f32_16x16x128_f8f6f4 v[90:93], v[18:25], v[190:197], v[90:93], v188, v188 op_sel_hi:[0,0,0]
	v_mfma_scale_f32_16x16x128_f8f6f4 v[78:81], v[26:33], v[198:205], v[78:81], v188, v188 op_sel_hi:[0,0,0]
	v_mfma_scale_f32_16x16x128_f8f6f4 v[74:77], v[18:25], v[198:205], v[74:77], v188, v188 op_sel_hi:[0,0,0]
	v_mfma_scale_f32_16x16x128_f8f6f4 v[62:65], v[26:33], v[206:213], v[62:65], v188, v188 op_sel_hi:[0,0,0]
	v_mfma_scale_f32_16x16x128_f8f6f4 v[58:61], v[18:25], v[206:213], v[58:61], v188, v188 op_sel_hi:[0,0,0]
	v_mfma_scale_f32_16x16x128_f8f6f4 v[46:49], v[26:33], v[214:221], v[46:49], v188, v188 op_sel_hi:[0,0,0]
	v_mfma_scale_f32_16x16x128_f8f6f4 v[42:45], v[18:25], v[214:221], v[42:45], v188, v188 op_sel_hi:[0,0,0]
	v_mfma_scale_f32_16x16x128_f8f6f4 v[86:89], v[10:17], v[190:197], v[86:89], v188, v188 op_sel_hi:[0,0,0]
	v_mfma_scale_f32_16x16x128_f8f6f4 v[82:85], v[2:9], v[190:197], v[82:85], v188, v188 op_sel_hi:[0,0,0]
	v_mfma_scale_f32_16x16x128_f8f6f4 v[70:73], v[10:17], v[198:205], v[70:73], v188, v188 op_sel_hi:[0,0,0]
	v_mfma_scale_f32_16x16x128_f8f6f4 v[66:69], v[2:9], v[198:205], v[66:69], v188, v188 op_sel_hi:[0,0,0]
	v_mfma_scale_f32_16x16x128_f8f6f4 v[54:57], v[10:17], v[206:213], v[54:57], v188, v188 op_sel_hi:[0,0,0]
	v_mfma_scale_f32_16x16x128_f8f6f4 v[50:53], v[2:9], v[206:213], v[50:53], v188, v188 op_sel_hi:[0,0,0]
	v_mfma_scale_f32_16x16x128_f8f6f4 v[38:41], v[10:17], v[214:221], v[38:41], v188, v188 op_sel_hi:[0,0,0]
	v_mfma_scale_f32_16x16x128_f8f6f4 v[34:37], v[2:9], v[214:221], v[34:37], v188, v188 op_sel_hi:[0,0,0]
	s_barrier
.Lmid_1482:
	s_add_i32 s2, 0, 0x18000
	v_add_u32_e32 v0, s2, v183
	s_add_i32 s3, 0, 0x1c000
	ds_read_b128 v[2:5], v0
	ds_read_b128 v[6:9], v0 offset:1024
	ds_read_b128 v[10:13], v0 offset:2048
	ds_read_b128 v[14:17], v0 offset:3072
	v_add_u32_e32 v0, s3, v183
	ds_read_b128 v[18:21], v0
	ds_read_b128 v[22:25], v0 offset:1024
	ds_read_b128 v[26:29], v0 offset:2048
	ds_read_b128 v[30:33], v0 offset:3072
	s_add_u32 s0, s38, 0x40000
	s_addc_u32 s1, s39, 0
	s_mov_b32 m0, s50
	v_lshl_add_u64 v[222:223], s[0:1], 0, v[162:163]
	ds_read_b128 v[190:193], v187 offset:32768
	ds_read_b128 v[194:197], v187 offset:33792
	ds_read_b128 v[198:201], v187 offset:34816
	ds_read_b128 v[202:205], v187 offset:35840
	ds_read_b128 v[206:209], v187 offset:36864
	ds_read_b128 v[210:213], v187 offset:37888
	ds_read_b128 v[214:217], v187 offset:38912
	ds_read_b128 v[218:221], v187 offset:39936
	global_load_lds_dwordx4 v[222:223], off
	v_lshl_add_u64 v[222:223], s[0:1], 0, v[166:167]
	s_mov_b32 m0, s51
	s_nop 0
	global_load_lds_dwordx4 v[222:223], off
	s_waitcnt vmcnt(8)
	s_waitcnt lgkmcnt(0)
	s_barrier
	s_waitcnt lgkmcnt(0)
	v_mfma_scale_f32_16x16x128_f8f6f4 v[158:161], v[2:9], v[190:197], v[158:161], v188, v188 op_sel_hi:[0,0,0]
	v_mfma_scale_f32_16x16x128_f8f6f4 v[154:157], v[10:17], v[190:197], v[154:157], v188, v188 op_sel_hi:[0,0,0]
	v_mfma_scale_f32_16x16x128_f8f6f4 v[142:145], v[2:9], v[198:205], v[142:145], v188, v188 op_sel_hi:[0,0,0]
	v_mfma_scale_f32_16x16x128_f8f6f4 v[138:141], v[10:17], v[198:205], v[138:141], v188, v188 op_sel_hi:[0,0,0]
	v_mfma_scale_f32_16x16x128_f8f6f4 v[126:129], v[2:9], v[206:213], v[126:129], v188, v188 op_sel_hi:[0,0,0]
	v_mfma_scale_f32_16x16x128_f8f6f4 v[122:125], v[10:17], v[206:213], v[122:125], v188, v188 op_sel_hi:[0,0,0]
	v_mfma_scale_f32_16x16x128_f8f6f4 v[110:113], v[2:9], v[214:221], v[110:113], v188, v188 op_sel_hi:[0,0,0]
	v_mfma_scale_f32_16x16x128_f8f6f4 v[106:109], v[10:17], v[214:221], v[106:109], v188, v188 op_sel_hi:[0,0,0]
	v_mfma_scale_f32_16x16x128_f8f6f4 v[150:153], v[18:25], v[190:197], v[150:153], v188, v188 op_sel_hi:[0,0,0]
	v_mfma_scale_f32_16x16x128_f8f6f4 v[146:149], v[26:33], v[190:197], v[146:149], v188, v188 op_sel_hi:[0,0,0]
	v_mfma_scale_f32_16x16x128_f8f6f4 v[134:137], v[18:25], v[198:205], v[134:137], v188, v188 op_sel_hi:[0,0,0]
	v_mfma_scale_f32_16x16x128_f8f6f4 v[130:133], v[26:33], v[198:205], v[130:133], v188, v188 op_sel_hi:[0,0,0]
	v_mfma_scale_f32_16x16x128_f8f6f4 v[118:121], v[18:25], v[206:213], v[118:121], v188, v188 op_sel_hi:[0,0,0]
	v_mfma_scale_f32_16x16x128_f8f6f4 v[114:117], v[26:33], v[206:213], v[114:117], v188, v188 op_sel_hi:[0,0,0]
	v_mfma_scale_f32_16x16x128_f8f6f4 v[102:105], v[18:25], v[214:221], v[102:105], v188, v188 op_sel_hi:[0,0,0]
	v_mfma_scale_f32_16x16x128_f8f6f4 v[98:101], v[26:33], v[214:221], v[98:101], v188, v188 op_sel_hi:[0,0,0]
	s_barrier
	s_add_u32 s0, s36, 0x2000
	s_addc_u32 s1, s37, 0
	s_add_i32 s2, s2, s49
	v_lshl_add_u64 v[222:223], s[0:1], 0, v[164:165]
	s_mov_b32 m0, s2
	ds_read_b128 v[190:193], v187 offset:49152
	ds_read_b128 v[194:197], v187 offset:50176
	ds_read_b128 v[198:201], v187 offset:51200
	ds_read_b128 v[202:205], v187 offset:52224
	ds_read_b128 v[206:209], v187 offset:53248
	ds_read_b128 v[210:213], v187 offset:54272
	ds_read_b128 v[214:217], v187 offset:55296
	ds_read_b128 v[218:221], v187 offset:56320
	global_load_lds_dwordx4 v[222:223], off
	s_add_i32 m0, s2, 0x2000
	v_lshl_add_u64 v[222:223], s[0:1], 0, v[168:169]
	s_add_u32 s0, s36, 0x42000
	s_addc_u32 s1, s37, 0
	s_add_i32 s2, s3, s49
	global_load_lds_dwordx4 v[222:223], off
	v_lshl_add_u64 v[222:223], s[0:1], 0, v[164:165]
	s_mov_b32 m0, s2
	v_lshl_add_u64 v[178:179], v[178:179], 0, s[16:17]
	global_load_lds_dwordx4 v[222:223], off
	v_lshl_add_u64 v[222:223], s[0:1], 0, v[168:169]
	s_add_i32 m0, s2, 0x2000
	s_nop 0
	global_load_lds_dwordx4 v[222:223], off
	s_mov_b32 m0, s53
	s_nop 0
	global_load_lds_dwordx4 v[178:179], off
	v_lshl_add_u64 v[178:179], v[180:181], 0, s[16:17]
	s_mov_b32 m0, s54
	s_nop 0
	global_load_lds_dwordx4 v[178:179], off
	s_waitcnt vmcnt(8)
	s_waitcnt lgkmcnt(0)
	s_barrier
	s_waitcnt lgkmcnt(0)
	v_mfma_scale_f32_16x16x128_f8f6f4 v[94:97], v[2:9], v[190:197], v[94:97], v188, v188 op_sel_hi:[0,0,0]
	v_mfma_scale_f32_16x16x128_f8f6f4 v[90:93], v[10:17], v[190:197], v[90:93], v188, v188 op_sel_hi:[0,0,0]
	v_mfma_scale_f32_16x16x128_f8f6f4 v[78:81], v[2:9], v[198:205], v[78:81], v188, v188 op_sel_hi:[0,0,0]
	v_mfma_scale_f32_16x16x128_f8f6f4 v[74:77], v[10:17], v[198:205], v[74:77], v188, v188 op_sel_hi:[0,0,0]
	v_mfma_scale_f32_16x16x128_f8f6f4 v[62:65], v[2:9], v[206:213], v[62:65], v188, v188 op_sel_hi:[0,0,0]
	v_mfma_scale_f32_16x16x128_f8f6f4 v[58:61], v[10:17], v[206:213], v[58:61], v188, v188 op_sel_hi:[0,0,0]
	v_mfma_scale_f32_16x16x128_f8f6f4 v[46:49], v[2:9], v[214:221], v[46:49], v188, v188 op_sel_hi:[0,0,0]
	v_mfma_scale_f32_16x16x128_f8f6f4 v[42:45], v[10:17], v[214:221], v[42:45], v188, v188 op_sel_hi:[0,0,0]
	v_mfma_scale_f32_16x16x128_f8f6f4 v[86:89], v[18:25], v[190:197], v[86:89], v188, v188 op_sel_hi:[0,0,0]
	v_mfma_scale_f32_16x16x128_f8f6f4 v[82:85], v[26:33], v[190:197], v[82:85], v188, v188 op_sel_hi:[0,0,0]
	v_mfma_scale_f32_16x16x128_f8f6f4 v[70:73], v[18:25], v[198:205], v[70:73], v188, v188 op_sel_hi:[0,0,0]
	v_mfma_scale_f32_16x16x128_f8f6f4 v[66:69], v[26:33], v[198:205], v[66:69], v188, v188 op_sel_hi:[0,0,0]
	v_mfma_scale_f32_16x16x128_f8f6f4 v[54:57], v[18:25], v[206:213], v[54:57], v188, v188 op_sel_hi:[0,0,0]
	v_mfma_scale_f32_16x16x128_f8f6f4 v[50:53], v[26:33], v[206:213], v[50:53], v188, v188 op_sel_hi:[0,0,0]
	v_mfma_scale_f32_16x16x128_f8f6f4 v[38:41], v[18:25], v[214:221], v[38:41], v188, v188 op_sel_hi:[0,0,0]
	v_mfma_scale_f32_16x16x128_f8f6f4 v[34:37], v[26:33], v[214:221], v[34:37], v188, v188 op_sel_hi:[0,0,0]
	s_barrier
	s_add_i32 s67, s67, 2
	s_add_u32 s65, s65, 0x4000
	s_addc_u32 s66, s66, 0
	s_add_u32 s34, s34, 0x100
	s_addc_u32 s35, s35, 0
	s_cmp_gt_u32 s67, 13
	s_cbranch_scc0 .LBB0_1482
	s_and_b64 vcc, exec, s[18:19]
	s_cbranch_vccz .LBB0_1485
	s_barrier

.LBB0_1576:
	s_lshl_b32 s1, s38, 8
	s_ashr_i32 s0, s38, 3
	s_and_b32 s1, s1, 0x700
	v_or_b32_e32 v240, s1, v183
	s_ashr_i32 s1, s0, 31
	s_lshl_b64 s[0:1], s[0:1], 13
	s_add_u32 s2, s6, s0
	s_addc_u32 s3, s7, s1
	v_lshlrev_b32_e32 v240, 2, v240
	global_load_dwordx4 v[224:227], v240, s[2:3]
	global_load_dwordx4 v[228:231], v240, s[2:3] offset:16
	global_load_dwordx4 v[232:235], v240, s[2:3] offset:512
	global_load_dwordx4 v[236:239], v240, s[2:3] offset:528
	s_ashr_i32 s27, s26, 31
	s_lshl_b64 s[0:1], s[26:27], 19
	s_add_u32 s30, s49, s0
	s_addc_u32 s31, s50, s1
	s_and_b64 s[0:1], s[4:5], exec
	s_cselect_b32 s27, s31, s43
	s_cselect_b32 s39, s30, s42
	s_ashr_i32 s29, s28, 31
	s_lshl_b64 s[0:1], s[28:29], 19
	s_add_u32 s34, s51, s0
	s_addc_u32 s35, s52, s1
	s_and_b64 s[0:1], s[4:5], exec
	s_cselect_b32 s29, s35, s41
	s_cselect_b32 s68, s34, s40
	s_add_u32 s69, s40, 0x4000
	s_addc_u32 s70, s41, 0
	s_add_u32 s40, s42, 0x40080
	s_addc_u32 s41, s43, 0
	s_mov_b32 s71, -2
	ds_read_b128 v[26:29], v184
	ds_read_b128 v[30:33], v184 offset:1024
	ds_read_b128 v[18:21], v184 offset:2048
	ds_read_b128 v[22:25], v184 offset:3072
	ds_read_b128 v[10:13], v185
	ds_read_b128 v[14:17], v185 offset:1024
	ds_read_b128 v[2:5], v185 offset:2048
	ds_read_b128 v[6:9], v185 offset:3072
	s_add_u32 s0, s40, 0xfffc0080
	s_addc_u32 s1, s41, -1
	s_cmp_eq_u32 s71, 12
	s_cselect_b32 s45, s27, s1
	s_cselect_b32 s44, s39, s0
	s_cselect_b32 s43, s29, s70
	s_cselect_b32 s42, s68, s69
	v_lshl_add_u64 v[178:179], s[40:41], 0, v[172:173]
	s_add_i32 m0, s37, 0xc000
	ds_read_b128 v[188:191], v186
	ds_read_b128 v[192:195], v186 offset:1024
	ds_read_b128 v[196:199], v186 offset:2048
	ds_read_b128 v[200:203], v186 offset:3072
	ds_read_b128 v[204:207], v186 offset:4096
	ds_read_b128 v[208:211], v186 offset:5120
	ds_read_b128 v[212:215], v186 offset:6144
	ds_read_b128 v[216:219], v186 offset:7168
	global_load_lds_dwordx4 v[178:179], off
	v_lshl_add_u64 v[178:179], s[40:41], 0, v[174:175]
	s_add_i32 m0, s37, 0xe000
	s_nop 0
	global_load_lds_dwordx4 v[178:179], off
	s_waitcnt vmcnt(8)
	s_waitcnt lgkmcnt(0)
	s_barrier
	s_waitcnt lgkmcnt(0)
	v_mfma_scale_f32_16x16x128_f8f6f4 v[158:161], v[26:33], v[188:195], 0, v187, v187 op_sel_hi:[0,0,0]
	v_mfma_scale_f32_16x16x128_f8f6f4 v[154:157], v[18:25], v[188:195], 0, v187, v187 op_sel_hi:[0,0,0]
	v_mfma_scale_f32_16x16x128_f8f6f4 v[150:153], v[26:33], v[196:203], 0, v187, v187 op_sel_hi:[0,0,0]
	v_mfma_scale_f32_16x16x128_f8f6f4 v[146:149], v[18:25], v[196:203], 0, v187, v187 op_sel_hi:[0,0,0]
	v_mfma_scale_f32_16x16x128_f8f6f4 v[142:145], v[26:33], v[204:211], 0, v187, v187 op_sel_hi:[0,0,0]
	v_mfma_scale_f32_16x16x128_f8f6f4 v[138:141], v[18:25], v[204:211], 0, v187, v187 op_sel_hi:[0,0,0]
	v_mfma_scale_f32_16x16x128_f8f6f4 v[134:137], v[26:33], v[212:219], 0, v187, v187 op_sel_hi:[0,0,0]
	v_mfma_scale_f32_16x16x128_f8f6f4 v[130:133], v[18:25], v[212:219], 0, v187, v187 op_sel_hi:[0,0,0]
	v_mfma_scale_f32_16x16x128_f8f6f4 v[102:105], v[10:17], v[188:195], 0, v187, v187 op_sel_hi:[0,0,0]
	v_mfma_scale_f32_16x16x128_f8f6f4 v[98:101], v[2:9], v[188:195], 0, v187, v187 op_sel_hi:[0,0,0]
	v_mfma_scale_f32_16x16x128_f8f6f4 v[86:89], v[10:17], v[196:203], 0, v187, v187 op_sel_hi:[0,0,0]
	v_mfma_scale_f32_16x16x128_f8f6f4 v[82:85], v[2:9], v[196:203], 0, v187, v187 op_sel_hi:[0,0,0]
	v_mfma_scale_f32_16x16x128_f8f6f4 v[78:81], v[10:17], v[204:211], 0, v187, v187 op_sel_hi:[0,0,0]
	v_mfma_scale_f32_16x16x128_f8f6f4 v[74:77], v[2:9], v[204:211], 0, v187, v187 op_sel_hi:[0,0,0]
	v_mfma_scale_f32_16x16x128_f8f6f4 v[70:73], v[10:17], v[212:219], 0, v187, v187 op_sel_hi:[0,0,0]
	v_mfma_scale_f32_16x16x128_f8f6f4 v[66:69], v[2:9], v[212:219], 0, v187, v187 op_sel_hi:[0,0,0]
	s_barrier
	s_add_i32 s0, s62, s53
	v_lshl_add_u64 v[178:179], s[42:43], 0, v[164:165]
	s_mov_b32 m0, s0
	ds_read_b128 v[188:191], v186 offset:16384
	ds_read_b128 v[192:195], v186 offset:17408
	ds_read_b128 v[196:199], v186 offset:18432
	ds_read_b128 v[200:203], v186 offset:19456
	ds_read_b128 v[204:207], v186 offset:20480
	ds_read_b128 v[208:211], v186 offset:21504
	ds_read_b128 v[212:215], v186 offset:22528
	ds_read_b128 v[216:219], v186 offset:23552
	global_load_lds_dwordx4 v[178:179], off
	s_add_i32 m0, s0, 0x2000
	s_add_u32 s0, s42, 0x40000
	v_lshl_add_u64 v[178:179], s[42:43], 0, v[168:169]
	s_addc_u32 s1, s43, 0
	s_add_i32 s2, s63, s53
	global_load_lds_dwordx4 v[178:179], off
	v_lshl_add_u64 v[178:179], s[0:1], 0, v[164:165]
	s_mov_b32 m0, s2
	v_lshl_add_u64 v[180:181], s[44:45], 0, v[166:167]
	global_load_lds_dwordx4 v[178:179], off
	v_lshl_add_u64 v[178:179], s[0:1], 0, v[168:169]
	s_add_i32 m0, s2, 0x2000
	s_nop 0
	global_load_lds_dwordx4 v[178:179], off
	v_lshl_add_u64 v[178:179], s[44:45], 0, v[162:163]
	s_mov_b32 m0, s37
	s_nop 0
	global_load_lds_dwordx4 v[178:179], off
	s_mov_b32 m0, s54
	s_nop 0
	global_load_lds_dwordx4 v[180:181], off
	s_waitcnt vmcnt(8)
	s_waitcnt lgkmcnt(0)
	s_barrier
	s_waitcnt lgkmcnt(0)
	v_mfma_scale_f32_16x16x128_f8f6f4 v[126:129], v[26:33], v[188:195], 0, v187, v187 op_sel_hi:[0,0,0]
	v_mfma_scale_f32_16x16x128_f8f6f4 v[122:125], v[18:25], v[188:195], 0, v187, v187 op_sel_hi:[0,0,0]
	v_mfma_scale_f32_16x16x128_f8f6f4 v[118:121], v[26:33], v[196:203], 0, v187, v187 op_sel_hi:[0,0,0]
	v_mfma_scale_f32_16x16x128_f8f6f4 v[114:117], v[18:25], v[196:203], 0, v187, v187 op_sel_hi:[0,0,0]
	v_mfma_scale_f32_16x16x128_f8f6f4 v[110:113], v[26:33], v[204:211], 0, v187, v187 op_sel_hi:[0,0,0]
	v_mfma_scale_f32_16x16x128_f8f6f4 v[106:109], v[18:25], v[204:211], 0, v187, v187 op_sel_hi:[0,0,0]
	v_mfma_scale_f32_16x16x128_f8f6f4 v[94:97], v[26:33], v[212:219], 0, v187, v187 op_sel_hi:[0,0,0]
	v_mfma_scale_f32_16x16x128_f8f6f4 v[90:93], v[18:25], v[212:219], 0, v187, v187 op_sel_hi:[0,0,0]
	v_mfma_scale_f32_16x16x128_f8f6f4 v[62:65], v[10:17], v[188:195], 0, v187, v187 op_sel_hi:[0,0,0]
	v_mfma_scale_f32_16x16x128_f8f6f4 v[58:61], v[2:9], v[188:195], 0, v187, v187 op_sel_hi:[0,0,0]
	v_mfma_scale_f32_16x16x128_f8f6f4 v[54:57], v[10:17], v[196:203], 0, v187, v187 op_sel_hi:[0,0,0]
	v_mfma_scale_f32_16x16x128_f8f6f4 v[50:53], v[2:9], v[196:203], 0, v187, v187 op_sel_hi:[0,0,0]
	v_mfma_scale_f32_16x16x128_f8f6f4 v[46:49], v[10:17], v[204:211], 0, v187, v187 op_sel_hi:[0,0,0]
	v_mfma_scale_f32_16x16x128_f8f6f4 v[42:45], v[2:9], v[204:211], 0, v187, v187 op_sel_hi:[0,0,0]
	v_mfma_scale_f32_16x16x128_f8f6f4 v[38:41], v[10:17], v[212:219], 0, v187, v187 op_sel_hi:[0,0,0]
	v_mfma_scale_f32_16x16x128_f8f6f4 v[34:37], v[2:9], v[212:219], 0, v187, v187 op_sel_hi:[0,0,0]
	s_barrier
	s_branch .Lmid_1577
.LBB0_1577:
	ds_read_b128 v[26:29], v184
	ds_read_b128 v[30:33], v184 offset:1024
	ds_read_b128 v[18:21], v184 offset:2048
	ds_read_b128 v[22:25], v184 offset:3072
	ds_read_b128 v[10:13], v185
	ds_read_b128 v[14:17], v185 offset:1024
	ds_read_b128 v[2:5], v185 offset:2048
	ds_read_b128 v[6:9], v185 offset:3072
	s_add_u32 s0, s40, 0xfffc0080
	s_addc_u32 s1, s41, -1
	s_cmp_eq_u32 s71, 12
	s_cselect_b32 s45, s27, s1
	s_cselect_b32 s44, s39, s0
	s_cselect_b32 s43, s29, s70
	s_cselect_b32 s42, s68, s69
	v_lshl_add_u64 v[178:179], s[40:41], 0, v[172:173]
	s_add_i32 m0, s37, 0xc000
	ds_read_b128 v[188:191], v186
	ds_read_b128 v[192:195], v186 offset:1024
	ds_read_b128 v[196:199], v186 offset:2048
	ds_read_b128 v[200:203], v186 offset:3072
	ds_read_b128 v[204:207], v186 offset:4096
	ds_read_b128 v[208:211], v186 offset:5120
	ds_read_b128 v[212:215], v186 offset:6144
	ds_read_b128 v[216:219], v186 offset:7168
	global_load_lds_dwordx4 v[178:179], off
	v_lshl_add_u64 v[178:179], s[40:41], 0, v[174:175]
	s_add_i32 m0, s37, 0xe000
	s_nop 0
	global_load_lds_dwordx4 v[178:179], off
	s_waitcnt vmcnt(8)
	s_waitcnt lgkmcnt(0)
	s_barrier
	s_waitcnt lgkmcnt(0)
	v_mfma_scale_f32_16x16x128_f8f6f4 v[158:161], v[26:33], v[188:195], v[158:161], v187, v187 op_sel_hi:[0,0,0]
	v_mfma_scale_f32_16x16x128_f8f6f4 v[154:157], v[18:25], v[188:195], v[154:157], v187, v187 op_sel_hi:[0,0,0]
	v_mfma_scale_f32_16x16x128_f8f6f4 v[150:153], v[26:33], v[196:203], v[150:153], v187, v187 op_sel_hi:[0,0,0]
	v_mfma_scale_f32_16x16x128_f8f6f4 v[146:149], v[18:25], v[196:203], v[146:149], v187, v187 op_sel_hi:[0,0,0]
	v_mfma_scale_f32_16x16x128_f8f6f4 v[142:145], v[26:33], v[204:211], v[142:145], v187, v187 op_sel_hi:[0,0,0]
	v_mfma_scale_f32_16x16x128_f8f6f4 v[138:141], v[18:25], v[204:211], v[138:141], v187, v187 op_sel_hi:[0,0,0]
	v_mfma_scale_f32_16x16x128_f8f6f4 v[134:137], v[26:33], v[212:219], v[134:137], v187, v187 op_sel_hi:[0,0,0]
	v_mfma_scale_f32_16x16x128_f8f6f4 v[130:133], v[18:25], v[212:219], v[130:133], v187, v187 op_sel_hi:[0,0,0]
	v_mfma_scale_f32_16x16x128_f8f6f4 v[102:105], v[10:17], v[188:195], v[102:105], v187, v187 op_sel_hi:[0,0,0]
	v_mfma_scale_f32_16x16x128_f8f6f4 v[98:101], v[2:9], v[188:195], v[98:101], v187, v187 op_sel_hi:[0,0,0]
	v_mfma_scale_f32_16x16x128_f8f6f4 v[86:89], v[10:17], v[196:203], v[86:89], v187, v187 op_sel_hi:[0,0,0]
	v_mfma_scale_f32_16x16x128_f8f6f4 v[82:85], v[2:9], v[196:203], v[82:85], v187, v187 op_sel_hi:[0,0,0]
	v_mfma_scale_f32_16x16x128_f8f6f4 v[78:81], v[10:17], v[204:211], v[78:81], v187, v187 op_sel_hi:[0,0,0]
	v_mfma_scale_f32_16x16x128_f8f6f4 v[74:77], v[2:9], v[204:211], v[74:77], v187, v187 op_sel_hi:[0,0,0]
	v_mfma_scale_f32_16x16x128_f8f6f4 v[70:73], v[10:17], v[212:219], v[70:73], v187, v187 op_sel_hi:[0,0,0]
	v_mfma_scale_f32_16x16x128_f8f6f4 v[66:69], v[2:9], v[212:219], v[66:69], v187, v187 op_sel_hi:[0,0,0]
	s_barrier
	s_add_i32 s0, s62, s53
	v_lshl_add_u64 v[178:179], s[42:43], 0, v[164:165]
	s_mov_b32 m0, s0
	ds_read_b128 v[188:191], v186 offset:16384
	ds_read_b128 v[192:195], v186 offset:17408
	ds_read_b128 v[196:199], v186 offset:18432
	ds_read_b128 v[200:203], v186 offset:19456
	ds_read_b128 v[204:207], v186 offset:20480
	ds_read_b128 v[208:211], v186 offset:21504
	ds_read_b128 v[212:215], v186 offset:22528
	ds_read_b128 v[216:219], v186 offset:23552
	global_load_lds_dwordx4 v[178:179], off
	s_add_i32 m0, s0, 0x2000
	s_add_u32 s0, s42, 0x40000
	v_lshl_add_u64 v[178:179], s[42:43], 0, v[168:169]
	s_addc_u32 s1, s43, 0
	s_add_i32 s2, s63, s53
	global_load_lds_dwordx4 v[178:179], off
	v_lshl_add_u64 v[178:179], s[0:1], 0, v[164:165]
	s_mov_b32 m0, s2
	v_lshl_add_u64 v[180:181], s[44:45], 0, v[166:167]
	global_load_lds_dwordx4 v[178:179], off
	v_lshl_add_u64 v[178:179], s[0:1], 0, v[168:169]
	s_add_i32 m0, s2, 0x2000
	s_nop 0
	global_load_lds_dwordx4 v[178:179], off
	v_lshl_add_u64 v[178:179], s[44:45], 0, v[162:163]
	s_mov_b32 m0, s37
	s_nop 0
	global_load_lds_dwordx4 v[178:179], off
	s_mov_b32 m0, s54
	s_nop 0
	global_load_lds_dwordx4 v[180:181], off
	s_waitcnt vmcnt(8)
	s_waitcnt lgkmcnt(0)
	s_barrier
	s_waitcnt lgkmcnt(0)
	v_mfma_scale_f32_16x16x128_f8f6f4 v[126:129], v[26:33], v[188:195], v[126:129], v187, v187 op_sel_hi:[0,0,0]
	v_mfma_scale_f32_16x16x128_f8f6f4 v[122:125], v[18:25], v[188:195], v[122:125], v187, v187 op_sel_hi:[0,0,0]
	v_mfma_scale_f32_16x16x128_f8f6f4 v[118:121], v[26:33], v[196:203], v[118:121], v187, v187 op_sel_hi:[0,0,0]
	v_mfma_scale_f32_16x16x128_f8f6f4 v[114:117], v[18:25], v[196:203], v[114:117], v187, v187 op_sel_hi:[0,0,0]
	v_mfma_scale_f32_16x16x128_f8f6f4 v[110:113], v[26:33], v[204:211], v[110:113], v187, v187 op_sel_hi:[0,0,0]
	v_mfma_scale_f32_16x16x128_f8f6f4 v[106:109], v[18:25], v[204:211], v[106:109], v187, v187 op_sel_hi:[0,0,0]
	v_mfma_scale_f32_16x16x128_f8f6f4 v[94:97], v[26:33], v[212:219], v[94:97], v187, v187 op_sel_hi:[0,0,0]
	v_mfma_scale_f32_16x16x128_f8f6f4 v[90:93], v[18:25], v[212:219], v[90:93], v187, v187 op_sel_hi:[0,0,0]
	v_mfma_scale_f32_16x16x128_f8f6f4 v[62:65], v[10:17], v[188:195], v[62:65], v187, v187 op_sel_hi:[0,0,0]
	v_mfma_scale_f32_16x16x128_f8f6f4 v[58:61], v[2:9], v[188:195], v[58:61], v187, v187 op_sel_hi:[0,0,0]
	v_mfma_scale_f32_16x16x128_f8f6f4 v[54:57], v[10:17], v[196:203], v[54:57], v187, v187 op_sel_hi:[0,0,0]
	v_mfma_scale_f32_16x16x128_f8f6f4 v[50:53], v[2:9], v[196:203], v[50:53], v187, v187 op_sel_hi:[0,0,0]
	v_mfma_scale_f32_16x16x128_f8f6f4 v[46:49], v[10:17], v[204:211], v[46:49], v187, v187 op_sel_hi:[0,0,0]
	v_mfma_scale_f32_16x16x128_f8f6f4 v[42:45], v[2:9], v[204:211], v[42:45], v187, v187 op_sel_hi:[0,0,0]
	v_mfma_scale_f32_16x16x128_f8f6f4 v[38:41], v[10:17], v[212:219], v[38:41], v187, v187 op_sel_hi:[0,0,0]
	v_mfma_scale_f32_16x16x128_f8f6f4 v[34:37], v[2:9], v[212:219], v[34:37], v187, v187 op_sel_hi:[0,0,0]
	s_barrier
.Lmid_1577:
	s_add_i32 s2, 0, 0x18000
	v_add_u32_e32 v0, s2, v182
	s_add_i32 s3, 0, 0x1c000
	ds_read_b128 v[2:5], v0
	ds_read_b128 v[6:9], v0 offset:1024
	ds_read_b128 v[10:13], v0 offset:2048
	ds_read_b128 v[14:17], v0 offset:3072
	v_add_u32_e32 v0, s3, v182
	ds_read_b128 v[18:21], v0
	ds_read_b128 v[22:25], v0 offset:1024
	ds_read_b128 v[26:29], v0 offset:2048
	ds_read_b128 v[30:33], v0 offset:3072
	s_add_u32 s0, s44, 0x40000
	s_addc_u32 s1, s45, 0
	s_mov_b32 m0, s55
	v_lshl_add_u64 v[220:221], s[0:1], 0, v[162:163]
	ds_read_b128 v[188:191], v186 offset:32768
	ds_read_b128 v[192:195], v186 offset:33792
	ds_read_b128 v[196:199], v186 offset:34816
	ds_read_b128 v[200:203], v186 offset:35840
	ds_read_b128 v[204:207], v186 offset:36864
	ds_read_b128 v[208:211], v186 offset:37888
	ds_read_b128 v[212:215], v186 offset:38912
	ds_read_b128 v[216:219], v186 offset:39936
	global_load_lds_dwordx4 v[220:221], off
	v_lshl_add_u64 v[220:221], s[0:1], 0, v[166:167]
	s_mov_b32 m0, s56
	s_nop 0
	global_load_lds_dwordx4 v[220:221], off
	s_waitcnt vmcnt(8)
	s_waitcnt lgkmcnt(0)
	s_barrier
	s_waitcnt lgkmcnt(0)
	v_mfma_scale_f32_16x16x128_f8f6f4 v[158:161], v[2:9], v[188:195], v[158:161], v187, v187 op_sel_hi:[0,0,0]
	v_mfma_scale_f32_16x16x128_f8f6f4 v[154:157], v[10:17], v[188:195], v[154:157], v187, v187 op_sel_hi:[0,0,0]
	v_mfma_scale_f32_16x16x128_f8f6f4 v[150:153], v[2:9], v[196:203], v[150:153], v187, v187 op_sel_hi:[0,0,0]
	v_mfma_scale_f32_16x16x128_f8f6f4 v[146:149], v[10:17], v[196:203], v[146:149], v187, v187 op_sel_hi:[0,0,0]
	v_mfma_scale_f32_16x16x128_f8f6f4 v[142:145], v[2:9], v[204:211], v[142:145], v187, v187 op_sel_hi:[0,0,0]
	v_mfma_scale_f32_16x16x128_f8f6f4 v[138:141], v[10:17], v[204:211], v[138:141], v187, v187 op_sel_hi:[0,0,0]
	v_mfma_scale_f32_16x16x128_f8f6f4 v[134:137], v[2:9], v[212:219], v[134:137], v187, v187 op_sel_hi:[0,0,0]
	v_mfma_scale_f32_16x16x128_f8f6f4 v[130:133], v[10:17], v[212:219], v[130:133], v187, v187 op_sel_hi:[0,0,0]
	v_mfma_scale_f32_16x16x128_f8f6f4 v[102:105], v[18:25], v[188:195], v[102:105], v187, v187 op_sel_hi:[0,0,0]
	v_mfma_scale_f32_16x16x128_f8f6f4 v[98:101], v[26:33], v[188:195], v[98:101], v187, v187 op_sel_hi:[0,0,0]
	v_mfma_scale_f32_16x16x128_f8f6f4 v[86:89], v[18:25], v[196:203], v[86:89], v187, v187 op_sel_hi:[0,0,0]
	v_mfma_scale_f32_16x16x128_f8f6f4 v[82:85], v[26:33], v[196:203], v[82:85], v187, v187 op_sel_hi:[0,0,0]
	v_mfma_scale_f32_16x16x128_f8f6f4 v[78:81], v[18:25], v[204:211], v[78:81], v187, v187 op_sel_hi:[0,0,0]
	v_mfma_scale_f32_16x16x128_f8f6f4 v[74:77], v[26:33], v[204:211], v[74:77], v187, v187 op_sel_hi:[0,0,0]
	v_mfma_scale_f32_16x16x128_f8f6f4 v[70:73], v[18:25], v[212:219], v[70:73], v187, v187 op_sel_hi:[0,0,0]
	v_mfma_scale_f32_16x16x128_f8f6f4 v[66:69], v[26:33], v[212:219], v[66:69], v187, v187 op_sel_hi:[0,0,0]
	s_barrier
	s_add_u32 s0, s42, 0x2000
	s_addc_u32 s1, s43, 0
	s_add_i32 s2, s2, s53
	v_lshl_add_u64 v[220:221], s[0:1], 0, v[164:165]
	s_mov_b32 m0, s2
	ds_read_b128 v[188:191], v186 offset:49152
	ds_read_b128 v[192:195], v186 offset:50176
	ds_read_b128 v[196:199], v186 offset:51200
	ds_read_b128 v[200:203], v186 offset:52224
	ds_read_b128 v[204:207], v186 offset:53248
	ds_read_b128 v[208:211], v186 offset:54272
	ds_read_b128 v[212:215], v186 offset:55296
	ds_read_b128 v[216:219], v186 offset:56320
	global_load_lds_dwordx4 v[220:221], off
	s_add_i32 m0, s2, 0x2000
	v_lshl_add_u64 v[220:221], s[0:1], 0, v[168:169]
	s_add_u32 s0, s42, 0x42000
	s_addc_u32 s1, s43, 0
	s_add_i32 s2, s3, s53
	global_load_lds_dwordx4 v[220:221], off
	v_lshl_add_u64 v[220:221], s[0:1], 0, v[164:165]
	s_mov_b32 m0, s2
	v_lshl_add_u64 v[178:179], v[178:179], 0, s[14:15]
	global_load_lds_dwordx4 v[220:221], off
	v_lshl_add_u64 v[220:221], s[0:1], 0, v[168:169]
	s_add_i32 m0, s2, 0x2000
	s_nop 0
	global_load_lds_dwordx4 v[220:221], off
	s_mov_b32 m0, s58
	s_nop 0
	global_load_lds_dwordx4 v[178:179], off
	v_lshl_add_u64 v[178:179], v[180:181], 0, s[14:15]
	s_mov_b32 m0, s59
	s_nop 0
	global_load_lds_dwordx4 v[178:179], off
	s_waitcnt vmcnt(8)
	s_waitcnt lgkmcnt(0)
	s_barrier
	s_waitcnt lgkmcnt(0)
	v_mfma_scale_f32_16x16x128_f8f6f4 v[126:129], v[2:9], v[188:195], v[126:129], v187, v187 op_sel_hi:[0,0,0]
	v_mfma_scale_f32_16x16x128_f8f6f4 v[122:125], v[10:17], v[188:195], v[122:125], v187, v187 op_sel_hi:[0,0,0]
	v_mfma_scale_f32_16x16x128_f8f6f4 v[118:121], v[2:9], v[196:203], v[118:121], v187, v187 op_sel_hi:[0,0,0]
	v_mfma_scale_f32_16x16x128_f8f6f4 v[114:117], v[10:17], v[196:203], v[114:117], v187, v187 op_sel_hi:[0,0,0]
	v_mfma_scale_f32_16x16x128_f8f6f4 v[110:113], v[2:9], v[204:211], v[110:113], v187, v187 op_sel_hi:[0,0,0]
	v_mfma_scale_f32_16x16x128_f8f6f4 v[106:109], v[10:17], v[204:211], v[106:109], v187, v187 op_sel_hi:[0,0,0]
	v_mfma_scale_f32_16x16x128_f8f6f4 v[94:97], v[2:9], v[212:219], v[94:97], v187, v187 op_sel_hi:[0,0,0]
	v_mfma_scale_f32_16x16x128_f8f6f4 v[90:93], v[10:17], v[212:219], v[90:93], v187, v187 op_sel_hi:[0,0,0]
	v_mfma_scale_f32_16x16x128_f8f6f4 v[62:65], v[18:25], v[188:195], v[62:65], v187, v187 op_sel_hi:[0,0,0]
	v_mfma_scale_f32_16x16x128_f8f6f4 v[58:61], v[26:33], v[188:195], v[58:61], v187, v187 op_sel_hi:[0,0,0]
	v_mfma_scale_f32_16x16x128_f8f6f4 v[54:57], v[18:25], v[196:203], v[54:57], v187, v187 op_sel_hi:[0,0,0]
	v_mfma_scale_f32_16x16x128_f8f6f4 v[50:53], v[26:33], v[196:203], v[50:53], v187, v187 op_sel_hi:[0,0,0]
	v_mfma_scale_f32_16x16x128_f8f6f4 v[46:49], v[18:25], v[204:211], v[46:49], v187, v187 op_sel_hi:[0,0,0]
	v_mfma_scale_f32_16x16x128_f8f6f4 v[42:45], v[26:33], v[204:211], v[42:45], v187, v187 op_sel_hi:[0,0,0]
	v_mfma_scale_f32_16x16x128_f8f6f4 v[38:41], v[18:25], v[212:219], v[38:41], v187, v187 op_sel_hi:[0,0,0]
	v_mfma_scale_f32_16x16x128_f8f6f4 v[34:37], v[26:33], v[212:219], v[34:37], v187, v187 op_sel_hi:[0,0,0]
	s_barrier
	s_add_i32 s71, s71, 2
	s_add_u32 s69, s69, 0x4000
	s_addc_u32 s70, s70, 0
	s_add_u32 s40, s40, 0x100
	s_addc_u32 s41, s41, 0
	s_cmp_gt_u32 s71, 13
	s_cbranch_scc0 .LBB0_1577
	s_and_b64 vcc, exec, s[16:17]
	s_cbranch_vccz .LBB0_1580
	s_barrier
